# k_spatial rewritten by hand for 128 VGPRs so two workgroups share a CU: two-pass row max, per-block exp to fp16 P then PV, second pass writes attn_s
# speedup vs baseline: 1.0346x; 1.0346x over previous
_Z14k_qkv_temporalPKDF16_S0_PKfPDF16_S3_S3_PfPi:
	s_load_dwordx4 s[36:39], s[0:1], 0x0
	s_load_dwordx2 s[40:41], s[0:1], 0x10
	s_load_dwordx4 s[8:11], s[0:1], 0x30
	s_and_b32 s3, s2, 7
	s_mul_i32 s3, s3, 0x71
	s_lshr_b32 s4, s2, 3
	s_add_u32 s3, s3, s4
	s_and_b32 s22, s3, 7
	s_lshr_b32 s16, s3, 3
	s_mul_i32 s16, s16, 14
	v_lshrrev_b32_e32 v1, 6, v0
	v_and_b32_e32 v92, 15, v0
	v_bfe_u32 v90, v0, 4, 2
	v_lshlrev_b32_e32 v95, 2, v90
	v_lshl_or_b32 v91, v1, 5, v95
	v_bfe_u32 v162, v0, 3, 3
	v_and_b32_e32 v163, 7, v0
	v_lshrrev_b32_e32 v110, 1, v162
	v_and_b32_e32 v111, 1, v1
	v_lshl_or_b32 v110, v111, 2, v110
	v_xor_b32_e32 v110, v163, v110
	v_lshlrev_b32_e32 v110, 4, v110
	v_lshl_or_b32 v111, v1, 3, v162
	s_mov_b32 s42, 0x12492493
	s_movk_i32 s43, 0x627
	s_movk_i32 s44, 0x628
	v_add_u32_e32 v112, 0, v111
	v_min_u32_e32 v112, 0x7d, v112
	v_mul_hi_u32 v113, v112, s42
	v_mul_u32_u24_e32 v114, 14, v113
	v_sub_u32_e32 v114, v112, v114
	v_add_u32_e32 v114, s16, v114
	v_min_u32_e32 v114, s43, v114
	v_mad_u32_u24 v114, v113, s44, v114
	v_lshl_or_b32 v100, v114, 10, v110
	v_add_u32_e32 v112, 32, v111
	v_min_u32_e32 v112, 0x7d, v112
	v_mul_hi_u32 v113, v112, s42
	v_mul_u32_u24_e32 v114, 14, v113
	v_sub_u32_e32 v114, v112, v114
	v_add_u32_e32 v114, s16, v114
	v_min_u32_e32 v114, s43, v114
	v_mad_u32_u24 v114, v113, s44, v114
	v_lshl_or_b32 v101, v114, 10, v110
	v_add_u32_e32 v112, 64, v111
	v_min_u32_e32 v112, 0x7d, v112
	v_mul_hi_u32 v113, v112, s42
	v_mul_u32_u24_e32 v114, 14, v113
	v_sub_u32_e32 v114, v112, v114
	v_add_u32_e32 v114, s16, v114
	v_min_u32_e32 v114, s43, v114
	v_mad_u32_u24 v114, v113, s44, v114
	v_lshl_or_b32 v102, v114, 10, v110
	v_add_u32_e32 v112, 96, v111
	v_min_u32_e32 v112, 0x7d, v112
	v_mul_hi_u32 v113, v112, s42
	v_mul_u32_u24_e32 v114, 14, v113
	v_sub_u32_e32 v114, v112, v114
	v_add_u32_e32 v114, s16, v114
	v_min_u32_e32 v114, s43, v114
	v_mad_u32_u24 v114, v113, s44, v114
	v_lshl_or_b32 v103, v114, 10, v110
	s_lshl_b32 s45, s22, 6
	v_add_u32_e32 v112, s45, v111
	v_lshl_or_b32 v112, v112, 10, v110
	v_mov_b32_e32 v104, v112
	v_add_u32_e32 v105, 0x8000, v112
	v_add_u32_e32 v106, 0x80000, v112
	v_add_u32_e32 v107, 0x88000, v112
	v_add_u32_e32 v108, 0x100000, v112
	v_add_u32_e32 v109, 0x108000, v112
	v_lshlrev_b32_e32 v113, 10, v1
	s_nop 0
	v_readfirstlane_b32 s24, v113
	s_add_u32 s25, s24, 0x1000
	s_add_u32 s26, s24, 0x2000
	s_add_u32 s27, s24, 0x3000
	s_add_u32 s28, s24, 0x4000
	s_add_u32 s29, s24, 0x5000
	s_add_u32 s30, s24, 0x6000
	s_add_u32 s31, s24, 0x7000
	s_add_u32 s32, s24, 0x8000
	s_add_u32 s33, s24, 0x9000
	s_add_u32 s46, s24, 0xa000
	s_add_u32 s47, s25, 0xa000
	s_add_u32 s48, s26, 0xa000
	s_add_u32 s49, s27, 0xa000
	s_add_u32 s50, s28, 0xa000
	s_add_u32 s51, s29, 0xa000
	s_add_u32 s52, s30, 0xa000
	s_add_u32 s53, s31, 0xa000
	s_add_u32 s54, s32, 0xa000
	s_add_u32 s55, s33, 0xa000
	v_lshrrev_b32_e32 v113, 1, v92
	v_xor_b32_e32 v113, v90, v113
	v_lshlrev_b32_e32 v113, 4, v113
	v_lshl_or_b32 v160, v92, 7, v113
	v_xor_b32_e32 v161, 64, v160
	v_lshlrev_b32_e32 v114, 12, v1
	v_add_u32_e32 v158, v114, v160
	v_xor_b32_e32 v159, 64, v158
	v_lshl_add_u32 v114, s22, 6, v92
	v_lshlrev_b32_e32 v114, 2, v114
	v_add_u32_e32 v115, 0x1000, v114
	s_waitcnt lgkmcnt(0)
	global_load_dword v116, v114, s[40:41] offset:0
	global_load_dword v117, v114, s[40:41] offset:64
	global_load_dword v118, v114, s[40:41] offset:128
	global_load_dword v119, v114, s[40:41] offset:192
	global_load_dword v120, v114, s[40:41] offset:2048
	global_load_dword v121, v114, s[40:41] offset:2112
	global_load_dword v122, v114, s[40:41] offset:2176
	global_load_dword v123, v114, s[40:41] offset:2240
	global_load_dword v124, v115, s[40:41] offset:0
	global_load_dword v125, v115, s[40:41] offset:64
	global_load_dword v126, v115, s[40:41] offset:128
	global_load_dword v127, v115, s[40:41] offset:192
	s_mov_b32 m0, s24
	s_nop 0
	global_load_lds_dwordx4 v100, s[36:37]
	s_mov_b32 m0, s25
	s_nop 0
	global_load_lds_dwordx4 v101, s[36:37]
	s_mov_b32 m0, s26
	s_nop 0
	global_load_lds_dwordx4 v102, s[36:37]
	s_mov_b32 m0, s27
	s_nop 0
	global_load_lds_dwordx4 v103, s[36:37]
	s_mov_b32 m0, s28
	s_nop 0
	global_load_lds_dwordx4 v104, s[38:39]
	s_mov_b32 m0, s29
	s_nop 0
	global_load_lds_dwordx4 v105, s[38:39]
	s_mov_b32 m0, s30
	s_nop 0
	global_load_lds_dwordx4 v106, s[38:39]
	s_mov_b32 m0, s31
	s_nop 0
	global_load_lds_dwordx4 v107, s[38:39]
	s_mov_b32 m0, s32
	s_nop 0
	global_load_lds_dwordx4 v108, s[38:39]
	s_mov_b32 m0, s33
	s_nop 0
	global_load_lds_dwordx4 v109, s[38:39]
	s_add_u32 s36, s36, 0x80
	s_addc_u32 s37, s37, 0
	s_add_u32 s38, s38, 0x80
	s_addc_u32 s39, s39, 0
	s_waitcnt vmcnt(10)
	v_mov_b32_e32 v164, v116
	v_mov_b32_e32 v165, v116
	v_mov_b32_e32 v166, v116
	v_mov_b32_e32 v167, v116
	v_mov_b32_e32 v62, v116
	v_mov_b32_e32 v63, v116
	v_mov_b32_e32 v64, v116
	v_mov_b32_e32 v65, v116
	v_mov_b32_e32 v86, v117
	v_mov_b32_e32 v87, v117
	v_mov_b32_e32 v88, v117
	v_mov_b32_e32 v89, v117
	v_mov_b32_e32 v58, v117
	v_mov_b32_e32 v59, v117
	v_mov_b32_e32 v60, v117
	v_mov_b32_e32 v61, v117
	v_mov_b32_e32 v96, v118
	v_mov_b32_e32 v97, v118
	v_mov_b32_e32 v98, v118
	v_mov_b32_e32 v99, v118
	v_mov_b32_e32 v54, v118
	v_mov_b32_e32 v55, v118
	v_mov_b32_e32 v56, v118
	v_mov_b32_e32 v57, v118
	v_mov_b32_e32 v82, v119
	v_mov_b32_e32 v83, v119
	v_mov_b32_e32 v84, v119
	v_mov_b32_e32 v85, v119
	v_mov_b32_e32 v50, v119
	v_mov_b32_e32 v51, v119
	v_mov_b32_e32 v52, v119
	v_mov_b32_e32 v53, v119
	v_mov_b32_e32 v78, v120
	v_mov_b32_e32 v79, v120
	v_mov_b32_e32 v80, v120
	v_mov_b32_e32 v81, v120
	v_mov_b32_e32 v46, v120
	v_mov_b32_e32 v47, v120
	v_mov_b32_e32 v48, v120
	v_mov_b32_e32 v49, v120
	v_mov_b32_e32 v74, v121
	v_mov_b32_e32 v75, v121
	v_mov_b32_e32 v76, v121
	v_mov_b32_e32 v77, v121
	v_mov_b32_e32 v42, v121
	v_mov_b32_e32 v43, v121
	v_mov_b32_e32 v44, v121
	v_mov_b32_e32 v45, v121
	v_mov_b32_e32 v70, v122
	v_mov_b32_e32 v71, v122
	v_mov_b32_e32 v72, v122
	v_mov_b32_e32 v73, v122
	v_mov_b32_e32 v38, v122
	v_mov_b32_e32 v39, v122
	v_mov_b32_e32 v40, v122
	v_mov_b32_e32 v41, v122
	v_mov_b32_e32 v66, v123
	v_mov_b32_e32 v67, v123
	v_mov_b32_e32 v68, v123
	v_mov_b32_e32 v69, v123
	v_mov_b32_e32 v34, v123
	v_mov_b32_e32 v35, v123
	v_mov_b32_e32 v36, v123
	v_mov_b32_e32 v37, v123
	v_mov_b32_e32 v18, v124
	v_mov_b32_e32 v19, v124
	v_mov_b32_e32 v20, v124
	v_mov_b32_e32 v21, v124
	v_mov_b32_e32 v2, v124
	v_mov_b32_e32 v3, v124
	v_mov_b32_e32 v4, v124
	v_mov_b32_e32 v5, v124
	v_mov_b32_e32 v26, v125
	v_mov_b32_e32 v27, v125
	v_mov_b32_e32 v28, v125
	v_mov_b32_e32 v29, v125
	v_mov_b32_e32 v10, v125
	v_mov_b32_e32 v11, v125
	v_mov_b32_e32 v12, v125
	v_mov_b32_e32 v13, v125
	v_mov_b32_e32 v22, v126
	v_mov_b32_e32 v23, v126
	v_mov_b32_e32 v24, v126
	v_mov_b32_e32 v25, v126
	v_mov_b32_e32 v6, v126
	v_mov_b32_e32 v7, v126
	v_mov_b32_e32 v8, v126
	v_mov_b32_e32 v9, v126
	v_mov_b32_e32 v30, v127
	v_mov_b32_e32 v31, v127
	v_mov_b32_e32 v32, v127
	v_mov_b32_e32 v33, v127
	v_mov_b32_e32 v14, v127
	v_mov_b32_e32 v15, v127
	v_mov_b32_e32 v16, v127
	v_mov_b32_e32 v17, v127
	s_waitcnt vmcnt(0)
	s_barrier
	ds_read_b128 v[110:113], v158 offset:0
	ds_read_b128 v[114:117], v158 offset:2048
	ds_read_b128 v[118:121], v159 offset:0
	ds_read_b128 v[122:125], v159 offset:2048
	ds_read_b128 v[126:129], v160 offset:16384
	ds_read_b128 v[130:133], v160 offset:18432
	ds_read_b128 v[134:137], v160 offset:20480
	ds_read_b128 v[138:141], v160 offset:22528
	ds_read_b128 v[142:145], v160 offset:24576
	ds_read_b128 v[146:149], v160 offset:26624
	ds_read_b128 v[150:153], v160 offset:28672
	ds_read_b128 v[154:157], v160 offset:30720
	s_waitcnt lgkmcnt(7)
	v_mfma_f32_16x16x32_f16 v[164:167], v[110:113], v[126:129], v[164:167]
	v_mfma_f32_16x16x32_f16 v[62:65], v[114:117], v[126:129], v[62:65]
	ds_read_b128 v[126:129], v160 offset:32768
	s_waitcnt lgkmcnt(7)
	v_mfma_f32_16x16x32_f16 v[86:89], v[110:113], v[130:133], v[86:89]
	v_mfma_f32_16x16x32_f16 v[58:61], v[114:117], v[130:133], v[58:61]
	ds_read_b128 v[130:133], v160 offset:34816
	s_waitcnt lgkmcnt(7)
	v_mfma_f32_16x16x32_f16 v[96:99], v[110:113], v[134:137], v[96:99]
	v_mfma_f32_16x16x32_f16 v[54:57], v[114:117], v[134:137], v[54:57]
	ds_read_b128 v[134:137], v160 offset:36864
	s_waitcnt lgkmcnt(7)
	v_mfma_f32_16x16x32_f16 v[82:85], v[110:113], v[138:141], v[82:85]
	v_mfma_f32_16x16x32_f16 v[50:53], v[114:117], v[138:141], v[50:53]
	ds_read_b128 v[138:141], v160 offset:38912
	s_waitcnt lgkmcnt(7)
	v_mfma_f32_16x16x32_f16 v[78:81], v[110:113], v[142:145], v[78:81]
	v_mfma_f32_16x16x32_f16 v[46:49], v[114:117], v[142:145], v[46:49]
	ds_read_b128 v[142:145], v161 offset:16384
	s_waitcnt lgkmcnt(7)
	v_mfma_f32_16x16x32_f16 v[74:77], v[110:113], v[146:149], v[74:77]
	v_mfma_f32_16x16x32_f16 v[42:45], v[114:117], v[146:149], v[42:45]
	ds_read_b128 v[146:149], v161 offset:18432
	s_waitcnt lgkmcnt(7)
	v_mfma_f32_16x16x32_f16 v[70:73], v[110:113], v[150:153], v[70:73]
	v_mfma_f32_16x16x32_f16 v[38:41], v[114:117], v[150:153], v[38:41]
	ds_read_b128 v[150:153], v161 offset:20480
	s_waitcnt lgkmcnt(7)
	v_mfma_f32_16x16x32_f16 v[66:69], v[110:113], v[154:157], v[66:69]
	v_mfma_f32_16x16x32_f16 v[34:37], v[114:117], v[154:157], v[34:37]
	ds_read_b128 v[154:157], v161 offset:22528
	s_waitcnt lgkmcnt(7)
	v_mfma_f32_16x16x32_f16 v[18:21], v[110:113], v[126:129], v[18:21]
	v_mfma_f32_16x16x32_f16 v[2:5], v[114:117], v[126:129], v[2:5]
	ds_read_b128 v[126:129], v161 offset:24576
	s_waitcnt lgkmcnt(7)
	v_mfma_f32_16x16x32_f16 v[26:29], v[110:113], v[130:133], v[26:29]
	v_mfma_f32_16x16x32_f16 v[10:13], v[114:117], v[130:133], v[10:13]
	ds_read_b128 v[130:133], v161 offset:26624
	s_waitcnt lgkmcnt(7)
	v_mfma_f32_16x16x32_f16 v[22:25], v[110:113], v[134:137], v[22:25]
	v_mfma_f32_16x16x32_f16 v[6:9], v[114:117], v[134:137], v[6:9]
	ds_read_b128 v[134:137], v161 offset:28672
	s_waitcnt lgkmcnt(7)
	v_mfma_f32_16x16x32_f16 v[30:33], v[110:113], v[138:141], v[30:33]
	v_mfma_f32_16x16x32_f16 v[14:17], v[114:117], v[138:141], v[14:17]
	ds_read_b128 v[138:141], v161 offset:30720
	s_waitcnt lgkmcnt(7)
	v_mfma_f32_16x16x32_f16 v[164:167], v[118:121], v[142:145], v[164:167]
	v_mfma_f32_16x16x32_f16 v[62:65], v[122:125], v[142:145], v[62:65]
	ds_read_b128 v[142:145], v161 offset:32768
	s_waitcnt lgkmcnt(7)
	v_mfma_f32_16x16x32_f16 v[86:89], v[118:121], v[146:149], v[86:89]
	v_mfma_f32_16x16x32_f16 v[58:61], v[122:125], v[146:149], v[58:61]
	ds_read_b128 v[146:149], v161 offset:34816
	s_waitcnt lgkmcnt(7)
	v_mfma_f32_16x16x32_f16 v[96:99], v[118:121], v[150:153], v[96:99]
	v_mfma_f32_16x16x32_f16 v[54:57], v[122:125], v[150:153], v[54:57]
	ds_read_b128 v[150:153], v161 offset:36864
	s_waitcnt lgkmcnt(7)
	v_mfma_f32_16x16x32_f16 v[82:85], v[118:121], v[154:157], v[82:85]
	v_mfma_f32_16x16x32_f16 v[50:53], v[122:125], v[154:157], v[50:53]
	ds_read_b128 v[154:157], v161 offset:38912
	s_waitcnt lgkmcnt(0)
	s_barrier
	s_mov_b32 m0, s24
	s_nop 0
	global_load_lds_dwordx4 v100, s[36:37]
	s_mov_b32 m0, s25
	s_nop 0
	global_load_lds_dwordx4 v101, s[36:37]
	s_mov_b32 m0, s26
	s_nop 0
	global_load_lds_dwordx4 v102, s[36:37]
	s_mov_b32 m0, s27
	s_nop 0
	global_load_lds_dwordx4 v103, s[36:37]
	s_mov_b32 m0, s28
	s_nop 0
	global_load_lds_dwordx4 v104, s[38:39]
	s_mov_b32 m0, s29
	s_nop 0
	global_load_lds_dwordx4 v105, s[38:39]
	s_mov_b32 m0, s30
	s_nop 0
	global_load_lds_dwordx4 v106, s[38:39]
	s_mov_b32 m0, s31
	s_nop 0
	global_load_lds_dwordx4 v107, s[38:39]
	s_mov_b32 m0, s32
	s_nop 0
	global_load_lds_dwordx4 v108, s[38:39]
	s_mov_b32 m0, s33
	s_nop 0
	global_load_lds_dwordx4 v109, s[38:39]
	s_add_u32 s36, s36, 0x80
	s_addc_u32 s37, s37, 0
	s_add_u32 s38, s38, 0x80
	s_addc_u32 s39, s39, 0
	s_waitcnt lgkmcnt(7)
	v_mfma_f32_16x16x32_f16 v[78:81], v[118:121], v[126:129], v[78:81]
	v_mfma_f32_16x16x32_f16 v[46:49], v[122:125], v[126:129], v[46:49]
	s_waitcnt lgkmcnt(6)
	v_mfma_f32_16x16x32_f16 v[74:77], v[118:121], v[130:133], v[74:77]
	v_mfma_f32_16x16x32_f16 v[42:45], v[122:125], v[130:133], v[42:45]
	s_waitcnt lgkmcnt(5)
	v_mfma_f32_16x16x32_f16 v[70:73], v[118:121], v[134:137], v[70:73]
	v_mfma_f32_16x16x32_f16 v[38:41], v[122:125], v[134:137], v[38:41]
	s_waitcnt lgkmcnt(4)
	v_mfma_f32_16x16x32_f16 v[66:69], v[118:121], v[138:141], v[66:69]
	v_mfma_f32_16x16x32_f16 v[34:37], v[122:125], v[138:141], v[34:37]
	s_waitcnt lgkmcnt(3)
	v_mfma_f32_16x16x32_f16 v[18:21], v[118:121], v[142:145], v[18:21]
	v_mfma_f32_16x16x32_f16 v[2:5], v[122:125], v[142:145], v[2:5]
	s_waitcnt lgkmcnt(2)
	v_mfma_f32_16x16x32_f16 v[26:29], v[118:121], v[146:149], v[26:29]
	v_mfma_f32_16x16x32_f16 v[10:13], v[122:125], v[146:149], v[10:13]
	s_waitcnt lgkmcnt(1)
	v_mfma_f32_16x16x32_f16 v[22:25], v[118:121], v[150:153], v[22:25]
	v_mfma_f32_16x16x32_f16 v[6:9], v[122:125], v[150:153], v[6:9]
	s_waitcnt lgkmcnt(0)
	v_mfma_f32_16x16x32_f16 v[30:33], v[118:121], v[154:157], v[30:33]
	v_mfma_f32_16x16x32_f16 v[14:17], v[122:125], v[154:157], v[14:17]
	s_waitcnt vmcnt(0)
	s_barrier
	ds_read_b128 v[110:113], v158 offset:0
	ds_read_b128 v[114:117], v158 offset:2048
	ds_read_b128 v[118:121], v159 offset:0
	ds_read_b128 v[122:125], v159 offset:2048
	ds_read_b128 v[126:129], v160 offset:16384
	ds_read_b128 v[130:133], v160 offset:18432
	ds_read_b128 v[134:137], v160 offset:20480
	ds_read_b128 v[138:141], v160 offset:22528
	ds_read_b128 v[142:145], v160 offset:24576
	ds_read_b128 v[146:149], v160 offset:26624
	ds_read_b128 v[150:153], v160 offset:28672
	ds_read_b128 v[154:157], v160 offset:30720
	s_waitcnt lgkmcnt(7)
	v_mfma_f32_16x16x32_f16 v[164:167], v[110:113], v[126:129], v[164:167]
	v_mfma_f32_16x16x32_f16 v[62:65], v[114:117], v[126:129], v[62:65]
	ds_read_b128 v[126:129], v160 offset:32768
	s_waitcnt lgkmcnt(7)
	v_mfma_f32_16x16x32_f16 v[86:89], v[110:113], v[130:133], v[86:89]
	v_mfma_f32_16x16x32_f16 v[58:61], v[114:117], v[130:133], v[58:61]
	ds_read_b128 v[130:133], v160 offset:34816
	s_waitcnt lgkmcnt(7)
	v_mfma_f32_16x16x32_f16 v[96:99], v[110:113], v[134:137], v[96:99]
	v_mfma_f32_16x16x32_f16 v[54:57], v[114:117], v[134:137], v[54:57]
	ds_read_b128 v[134:137], v160 offset:36864
	s_waitcnt lgkmcnt(7)
	v_mfma_f32_16x16x32_f16 v[82:85], v[110:113], v[138:141], v[82:85]
	v_mfma_f32_16x16x32_f16 v[50:53], v[114:117], v[138:141], v[50:53]
	ds_read_b128 v[138:141], v160 offset:38912
	s_waitcnt lgkmcnt(7)
	v_mfma_f32_16x16x32_f16 v[78:81], v[110:113], v[142:145], v[78:81]
	v_mfma_f32_16x16x32_f16 v[46:49], v[114:117], v[142:145], v[46:49]
	ds_read_b128 v[142:145], v161 offset:16384
	s_waitcnt lgkmcnt(7)
	v_mfma_f32_16x16x32_f16 v[74:77], v[110:113], v[146:149], v[74:77]
	v_mfma_f32_16x16x32_f16 v[42:45], v[114:117], v[146:149], v[42:45]
	ds_read_b128 v[146:149], v161 offset:18432
	s_waitcnt lgkmcnt(7)
	v_mfma_f32_16x16x32_f16 v[70:73], v[110:113], v[150:153], v[70:73]
	v_mfma_f32_16x16x32_f16 v[38:41], v[114:117], v[150:153], v[38:41]
	ds_read_b128 v[150:153], v161 offset:20480
	s_waitcnt lgkmcnt(7)
	v_mfma_f32_16x16x32_f16 v[66:69], v[110:113], v[154:157], v[66:69]
	v_mfma_f32_16x16x32_f16 v[34:37], v[114:117], v[154:157], v[34:37]
	ds_read_b128 v[154:157], v161 offset:22528
	s_waitcnt lgkmcnt(7)
	v_mfma_f32_16x16x32_f16 v[18:21], v[110:113], v[126:129], v[18:21]
	v_mfma_f32_16x16x32_f16 v[2:5], v[114:117], v[126:129], v[2:5]
	ds_read_b128 v[126:129], v161 offset:24576
	s_waitcnt lgkmcnt(7)
	v_mfma_f32_16x16x32_f16 v[26:29], v[110:113], v[130:133], v[26:29]
	v_mfma_f32_16x16x32_f16 v[10:13], v[114:117], v[130:133], v[10:13]
	ds_read_b128 v[130:133], v161 offset:26624
	s_waitcnt lgkmcnt(7)
	v_mfma_f32_16x16x32_f16 v[22:25], v[110:113], v[134:137], v[22:25]
	v_mfma_f32_16x16x32_f16 v[6:9], v[114:117], v[134:137], v[6:9]
	ds_read_b128 v[134:137], v161 offset:28672
	s_waitcnt lgkmcnt(7)
	v_mfma_f32_16x16x32_f16 v[30:33], v[110:113], v[138:141], v[30:33]
	v_mfma_f32_16x16x32_f16 v[14:17], v[114:117], v[138:141], v[14:17]
	ds_read_b128 v[138:141], v161 offset:30720
	s_waitcnt lgkmcnt(7)
	v_mfma_f32_16x16x32_f16 v[164:167], v[118:121], v[142:145], v[164:167]
	v_mfma_f32_16x16x32_f16 v[62:65], v[122:125], v[142:145], v[62:65]
	ds_read_b128 v[142:145], v161 offset:32768
	s_waitcnt lgkmcnt(7)
	v_mfma_f32_16x16x32_f16 v[86:89], v[118:121], v[146:149], v[86:89]
	v_mfma_f32_16x16x32_f16 v[58:61], v[122:125], v[146:149], v[58:61]
	ds_read_b128 v[146:149], v161 offset:34816
	s_waitcnt lgkmcnt(7)
	v_mfma_f32_16x16x32_f16 v[96:99], v[118:121], v[150:153], v[96:99]
	v_mfma_f32_16x16x32_f16 v[54:57], v[122:125], v[150:153], v[54:57]
	ds_read_b128 v[150:153], v161 offset:36864
	s_waitcnt lgkmcnt(7)
	v_mfma_f32_16x16x32_f16 v[82:85], v[118:121], v[154:157], v[82:85]
	v_mfma_f32_16x16x32_f16 v[50:53], v[122:125], v[154:157], v[50:53]
	ds_read_b128 v[154:157], v161 offset:38912
	s_waitcnt lgkmcnt(0)
	s_barrier
	s_mov_b32 m0, s24
	s_nop 0
	global_load_lds_dwordx4 v100, s[36:37]
	s_mov_b32 m0, s25
	s_nop 0
	global_load_lds_dwordx4 v101, s[36:37]
	s_mov_b32 m0, s26
	s_nop 0
	global_load_lds_dwordx4 v102, s[36:37]
	s_mov_b32 m0, s27
	s_nop 0
	global_load_lds_dwordx4 v103, s[36:37]
	s_mov_b32 m0, s28
	s_nop 0
	global_load_lds_dwordx4 v104, s[38:39]
	s_mov_b32 m0, s29
	s_nop 0
	global_load_lds_dwordx4 v105, s[38:39]
	s_mov_b32 m0, s30
	s_nop 0
	global_load_lds_dwordx4 v106, s[38:39]
	s_mov_b32 m0, s31
	s_nop 0
	global_load_lds_dwordx4 v107, s[38:39]
	s_mov_b32 m0, s32
	s_nop 0
	global_load_lds_dwordx4 v108, s[38:39]
	s_mov_b32 m0, s33
	s_nop 0
	global_load_lds_dwordx4 v109, s[38:39]
	s_add_u32 s36, s36, 0x80
	s_addc_u32 s37, s37, 0
	s_add_u32 s38, s38, 0x80
	s_addc_u32 s39, s39, 0
	s_waitcnt lgkmcnt(7)
	v_mfma_f32_16x16x32_f16 v[78:81], v[118:121], v[126:129], v[78:81]
	v_mfma_f32_16x16x32_f16 v[46:49], v[122:125], v[126:129], v[46:49]
	s_waitcnt lgkmcnt(6)
	v_mfma_f32_16x16x32_f16 v[74:77], v[118:121], v[130:133], v[74:77]
	v_mfma_f32_16x16x32_f16 v[42:45], v[122:125], v[130:133], v[42:45]
	s_waitcnt lgkmcnt(5)
	v_mfma_f32_16x16x32_f16 v[70:73], v[118:121], v[134:137], v[70:73]
	v_mfma_f32_16x16x32_f16 v[38:41], v[122:125], v[134:137], v[38:41]
	s_waitcnt lgkmcnt(4)
	v_mfma_f32_16x16x32_f16 v[66:69], v[118:121], v[138:141], v[66:69]
	v_mfma_f32_16x16x32_f16 v[34:37], v[122:125], v[138:141], v[34:37]
	s_waitcnt lgkmcnt(3)
	v_mfma_f32_16x16x32_f16 v[18:21], v[118:121], v[142:145], v[18:21]
	v_mfma_f32_16x16x32_f16 v[2:5], v[122:125], v[142:145], v[2:5]
	s_waitcnt lgkmcnt(2)
	v_mfma_f32_16x16x32_f16 v[26:29], v[118:121], v[146:149], v[26:29]
	v_mfma_f32_16x16x32_f16 v[10:13], v[122:125], v[146:149], v[10:13]
	s_waitcnt lgkmcnt(1)
	v_mfma_f32_16x16x32_f16 v[22:25], v[118:121], v[150:153], v[22:25]
	v_mfma_f32_16x16x32_f16 v[6:9], v[122:125], v[150:153], v[6:9]
	s_waitcnt lgkmcnt(0)
	v_mfma_f32_16x16x32_f16 v[30:33], v[118:121], v[154:157], v[30:33]
	v_mfma_f32_16x16x32_f16 v[14:17], v[122:125], v[154:157], v[14:17]
	s_waitcnt vmcnt(0)
	s_barrier
	ds_read_b128 v[110:113], v158 offset:0
	ds_read_b128 v[114:117], v158 offset:2048
	ds_read_b128 v[118:121], v159 offset:0
	ds_read_b128 v[122:125], v159 offset:2048
	ds_read_b128 v[126:129], v160 offset:16384
	ds_read_b128 v[130:133], v160 offset:18432
	ds_read_b128 v[134:137], v160 offset:20480
	ds_read_b128 v[138:141], v160 offset:22528
	ds_read_b128 v[142:145], v160 offset:24576
	ds_read_b128 v[146:149], v160 offset:26624
	ds_read_b128 v[150:153], v160 offset:28672
	ds_read_b128 v[154:157], v160 offset:30720
	s_waitcnt lgkmcnt(7)
	v_mfma_f32_16x16x32_f16 v[164:167], v[110:113], v[126:129], v[164:167]
	v_mfma_f32_16x16x32_f16 v[62:65], v[114:117], v[126:129], v[62:65]
	ds_read_b128 v[126:129], v160 offset:32768
	s_waitcnt lgkmcnt(7)
	v_mfma_f32_16x16x32_f16 v[86:89], v[110:113], v[130:133], v[86:89]
	v_mfma_f32_16x16x32_f16 v[58:61], v[114:117], v[130:133], v[58:61]
	ds_read_b128 v[130:133], v160 offset:34816
	s_waitcnt lgkmcnt(7)
	v_mfma_f32_16x16x32_f16 v[96:99], v[110:113], v[134:137], v[96:99]
	v_mfma_f32_16x16x32_f16 v[54:57], v[114:117], v[134:137], v[54:57]
	ds_read_b128 v[134:137], v160 offset:36864
	s_waitcnt lgkmcnt(7)
	v_mfma_f32_16x16x32_f16 v[82:85], v[110:113], v[138:141], v[82:85]
	v_mfma_f32_16x16x32_f16 v[50:53], v[114:117], v[138:141], v[50:53]
	ds_read_b128 v[138:141], v160 offset:38912
	s_waitcnt lgkmcnt(7)
	v_mfma_f32_16x16x32_f16 v[78:81], v[110:113], v[142:145], v[78:81]
	v_mfma_f32_16x16x32_f16 v[46:49], v[114:117], v[142:145], v[46:49]
	ds_read_b128 v[142:145], v161 offset:16384
	s_waitcnt lgkmcnt(7)
	v_mfma_f32_16x16x32_f16 v[74:77], v[110:113], v[146:149], v[74:77]
	v_mfma_f32_16x16x32_f16 v[42:45], v[114:117], v[146:149], v[42:45]
	ds_read_b128 v[146:149], v161 offset:18432
	s_waitcnt lgkmcnt(7)
	v_mfma_f32_16x16x32_f16 v[70:73], v[110:113], v[150:153], v[70:73]
	v_mfma_f32_16x16x32_f16 v[38:41], v[114:117], v[150:153], v[38:41]
	ds_read_b128 v[150:153], v161 offset:20480
	s_waitcnt lgkmcnt(7)
	v_mfma_f32_16x16x32_f16 v[66:69], v[110:113], v[154:157], v[66:69]
	v_mfma_f32_16x16x32_f16 v[34:37], v[114:117], v[154:157], v[34:37]
	ds_read_b128 v[154:157], v161 offset:22528
	s_waitcnt lgkmcnt(7)
	v_mfma_f32_16x16x32_f16 v[18:21], v[110:113], v[126:129], v[18:21]
	v_mfma_f32_16x16x32_f16 v[2:5], v[114:117], v[126:129], v[2:5]
	ds_read_b128 v[126:129], v161 offset:24576
	s_waitcnt lgkmcnt(7)
	v_mfma_f32_16x16x32_f16 v[26:29], v[110:113], v[130:133], v[26:29]
	v_mfma_f32_16x16x32_f16 v[10:13], v[114:117], v[130:133], v[10:13]
	ds_read_b128 v[130:133], v161 offset:26624
	s_waitcnt lgkmcnt(7)
	v_mfma_f32_16x16x32_f16 v[22:25], v[110:113], v[134:137], v[22:25]
	v_mfma_f32_16x16x32_f16 v[6:9], v[114:117], v[134:137], v[6:9]
	ds_read_b128 v[134:137], v161 offset:28672
	s_waitcnt lgkmcnt(7)
	v_mfma_f32_16x16x32_f16 v[30:33], v[110:113], v[138:141], v[30:33]
	v_mfma_f32_16x16x32_f16 v[14:17], v[114:117], v[138:141], v[14:17]
	ds_read_b128 v[138:141], v161 offset:30720
	s_waitcnt lgkmcnt(7)
	v_mfma_f32_16x16x32_f16 v[164:167], v[118:121], v[142:145], v[164:167]
	v_mfma_f32_16x16x32_f16 v[62:65], v[122:125], v[142:145], v[62:65]
	ds_read_b128 v[142:145], v161 offset:32768
	s_waitcnt lgkmcnt(7)
	v_mfma_f32_16x16x32_f16 v[86:89], v[118:121], v[146:149], v[86:89]
	v_mfma_f32_16x16x32_f16 v[58:61], v[122:125], v[146:149], v[58:61]
	ds_read_b128 v[146:149], v161 offset:34816
	s_waitcnt lgkmcnt(7)
	v_mfma_f32_16x16x32_f16 v[96:99], v[118:121], v[150:153], v[96:99]
	v_mfma_f32_16x16x32_f16 v[54:57], v[122:125], v[150:153], v[54:57]
	ds_read_b128 v[150:153], v161 offset:36864
	s_waitcnt lgkmcnt(7)
	v_mfma_f32_16x16x32_f16 v[82:85], v[118:121], v[154:157], v[82:85]
	v_mfma_f32_16x16x32_f16 v[50:53], v[122:125], v[154:157], v[50:53]
	ds_read_b128 v[154:157], v161 offset:38912
	s_waitcnt lgkmcnt(0)
	s_barrier
	s_mov_b32 m0, s24
	s_nop 0
	global_load_lds_dwordx4 v100, s[36:37]
	s_mov_b32 m0, s25
	s_nop 0
	global_load_lds_dwordx4 v101, s[36:37]
	s_mov_b32 m0, s26
	s_nop 0
	global_load_lds_dwordx4 v102, s[36:37]
	s_mov_b32 m0, s27
	s_nop 0
	global_load_lds_dwordx4 v103, s[36:37]
	s_mov_b32 m0, s28
	s_nop 0
	global_load_lds_dwordx4 v104, s[38:39]
	s_mov_b32 m0, s29
	s_nop 0
	global_load_lds_dwordx4 v105, s[38:39]
	s_mov_b32 m0, s30
	s_nop 0
	global_load_lds_dwordx4 v106, s[38:39]
	s_mov_b32 m0, s31
	s_nop 0
	global_load_lds_dwordx4 v107, s[38:39]
	s_mov_b32 m0, s32
	s_nop 0
	global_load_lds_dwordx4 v108, s[38:39]
	s_mov_b32 m0, s33
	s_nop 0
	global_load_lds_dwordx4 v109, s[38:39]
	s_add_u32 s36, s36, 0x80
	s_addc_u32 s37, s37, 0
	s_add_u32 s38, s38, 0x80
	s_addc_u32 s39, s39, 0
	s_waitcnt lgkmcnt(7)
	v_mfma_f32_16x16x32_f16 v[78:81], v[118:121], v[126:129], v[78:81]
	v_mfma_f32_16x16x32_f16 v[46:49], v[122:125], v[126:129], v[46:49]
	s_waitcnt lgkmcnt(6)
	v_mfma_f32_16x16x32_f16 v[74:77], v[118:121], v[130:133], v[74:77]
	v_mfma_f32_16x16x32_f16 v[42:45], v[122:125], v[130:133], v[42:45]
	s_waitcnt lgkmcnt(5)
	v_mfma_f32_16x16x32_f16 v[70:73], v[118:121], v[134:137], v[70:73]
	v_mfma_f32_16x16x32_f16 v[38:41], v[122:125], v[134:137], v[38:41]
	s_waitcnt lgkmcnt(4)
	v_mfma_f32_16x16x32_f16 v[66:69], v[118:121], v[138:141], v[66:69]
	v_mfma_f32_16x16x32_f16 v[34:37], v[122:125], v[138:141], v[34:37]
	s_waitcnt lgkmcnt(3)
	v_mfma_f32_16x16x32_f16 v[18:21], v[118:121], v[142:145], v[18:21]
	v_mfma_f32_16x16x32_f16 v[2:5], v[122:125], v[142:145], v[2:5]
	s_waitcnt lgkmcnt(2)
	v_mfma_f32_16x16x32_f16 v[26:29], v[118:121], v[146:149], v[26:29]
	v_mfma_f32_16x16x32_f16 v[10:13], v[122:125], v[146:149], v[10:13]
	s_waitcnt lgkmcnt(1)
	v_mfma_f32_16x16x32_f16 v[22:25], v[118:121], v[150:153], v[22:25]
	v_mfma_f32_16x16x32_f16 v[6:9], v[122:125], v[150:153], v[6:9]
	s_waitcnt lgkmcnt(0)
	v_mfma_f32_16x16x32_f16 v[30:33], v[118:121], v[154:157], v[30:33]
	v_mfma_f32_16x16x32_f16 v[14:17], v[122:125], v[154:157], v[14:17]
	s_waitcnt vmcnt(0)
	s_barrier
	ds_read_b128 v[110:113], v158 offset:0
	ds_read_b128 v[114:117], v158 offset:2048
	ds_read_b128 v[118:121], v159 offset:0
	ds_read_b128 v[122:125], v159 offset:2048
	ds_read_b128 v[126:129], v160 offset:16384
	ds_read_b128 v[130:133], v160 offset:18432
	ds_read_b128 v[134:137], v160 offset:20480
	ds_read_b128 v[138:141], v160 offset:22528
	ds_read_b128 v[142:145], v160 offset:24576
	ds_read_b128 v[146:149], v160 offset:26624
	ds_read_b128 v[150:153], v160 offset:28672
	ds_read_b128 v[154:157], v160 offset:30720
	s_waitcnt lgkmcnt(7)
	v_mfma_f32_16x16x32_f16 v[164:167], v[110:113], v[126:129], v[164:167]
	v_mfma_f32_16x16x32_f16 v[62:65], v[114:117], v[126:129], v[62:65]
	ds_read_b128 v[126:129], v160 offset:32768
	s_waitcnt lgkmcnt(7)
	v_mfma_f32_16x16x32_f16 v[86:89], v[110:113], v[130:133], v[86:89]
	v_mfma_f32_16x16x32_f16 v[58:61], v[114:117], v[130:133], v[58:61]
	ds_read_b128 v[130:133], v160 offset:34816
	s_waitcnt lgkmcnt(7)
	v_mfma_f32_16x16x32_f16 v[96:99], v[110:113], v[134:137], v[96:99]
	v_mfma_f32_16x16x32_f16 v[54:57], v[114:117], v[134:137], v[54:57]
	ds_read_b128 v[134:137], v160 offset:36864
	s_waitcnt lgkmcnt(7)
	v_mfma_f32_16x16x32_f16 v[82:85], v[110:113], v[138:141], v[82:85]
	v_mfma_f32_16x16x32_f16 v[50:53], v[114:117], v[138:141], v[50:53]
	ds_read_b128 v[138:141], v160 offset:38912
	s_waitcnt lgkmcnt(7)
	v_mfma_f32_16x16x32_f16 v[78:81], v[110:113], v[142:145], v[78:81]
	v_mfma_f32_16x16x32_f16 v[46:49], v[114:117], v[142:145], v[46:49]
	ds_read_b128 v[142:145], v161 offset:16384
	s_waitcnt lgkmcnt(7)
	v_mfma_f32_16x16x32_f16 v[74:77], v[110:113], v[146:149], v[74:77]
	v_mfma_f32_16x16x32_f16 v[42:45], v[114:117], v[146:149], v[42:45]
	ds_read_b128 v[146:149], v161 offset:18432
	s_waitcnt lgkmcnt(7)
	v_mfma_f32_16x16x32_f16 v[70:73], v[110:113], v[150:153], v[70:73]
	v_mfma_f32_16x16x32_f16 v[38:41], v[114:117], v[150:153], v[38:41]
	ds_read_b128 v[150:153], v161 offset:20480
	s_waitcnt lgkmcnt(7)
	v_mfma_f32_16x16x32_f16 v[66:69], v[110:113], v[154:157], v[66:69]
	v_mfma_f32_16x16x32_f16 v[34:37], v[114:117], v[154:157], v[34:37]
	ds_read_b128 v[154:157], v161 offset:22528
	s_waitcnt lgkmcnt(7)
	v_mfma_f32_16x16x32_f16 v[18:21], v[110:113], v[126:129], v[18:21]
	v_mfma_f32_16x16x32_f16 v[2:5], v[114:117], v[126:129], v[2:5]
	ds_read_b128 v[126:129], v161 offset:24576
	s_waitcnt lgkmcnt(7)
	v_mfma_f32_16x16x32_f16 v[26:29], v[110:113], v[130:133], v[26:29]
	v_mfma_f32_16x16x32_f16 v[10:13], v[114:117], v[130:133], v[10:13]
	ds_read_b128 v[130:133], v161 offset:26624
	s_waitcnt lgkmcnt(7)
	v_mfma_f32_16x16x32_f16 v[22:25], v[110:113], v[134:137], v[22:25]
	v_mfma_f32_16x16x32_f16 v[6:9], v[114:117], v[134:137], v[6:9]
	ds_read_b128 v[134:137], v161 offset:28672
	s_waitcnt lgkmcnt(7)
	v_mfma_f32_16x16x32_f16 v[30:33], v[110:113], v[138:141], v[30:33]
	v_mfma_f32_16x16x32_f16 v[14:17], v[114:117], v[138:141], v[14:17]
	ds_read_b128 v[138:141], v161 offset:30720
	s_waitcnt lgkmcnt(7)
	v_mfma_f32_16x16x32_f16 v[164:167], v[118:121], v[142:145], v[164:167]
	v_mfma_f32_16x16x32_f16 v[62:65], v[122:125], v[142:145], v[62:65]
	ds_read_b128 v[142:145], v161 offset:32768
	s_waitcnt lgkmcnt(7)
	v_mfma_f32_16x16x32_f16 v[86:89], v[118:121], v[146:149], v[86:89]
	v_mfma_f32_16x16x32_f16 v[58:61], v[122:125], v[146:149], v[58:61]
	ds_read_b128 v[146:149], v161 offset:34816
	s_waitcnt lgkmcnt(7)
	v_mfma_f32_16x16x32_f16 v[96:99], v[118:121], v[150:153], v[96:99]
	v_mfma_f32_16x16x32_f16 v[54:57], v[122:125], v[150:153], v[54:57]
	ds_read_b128 v[150:153], v161 offset:36864
	s_waitcnt lgkmcnt(7)
	v_mfma_f32_16x16x32_f16 v[82:85], v[118:121], v[154:157], v[82:85]
	v_mfma_f32_16x16x32_f16 v[50:53], v[122:125], v[154:157], v[50:53]
	ds_read_b128 v[154:157], v161 offset:38912
	s_waitcnt lgkmcnt(0)
	s_barrier
	s_mov_b32 m0, s24
	s_nop 0
	global_load_lds_dwordx4 v100, s[36:37]
	s_mov_b32 m0, s25
	s_nop 0
	global_load_lds_dwordx4 v101, s[36:37]
	s_mov_b32 m0, s26
	s_nop 0
	global_load_lds_dwordx4 v102, s[36:37]
	s_mov_b32 m0, s27
	s_nop 0
	global_load_lds_dwordx4 v103, s[36:37]
	s_mov_b32 m0, s28
	s_nop 0
	global_load_lds_dwordx4 v104, s[38:39]
	s_mov_b32 m0, s29
	s_nop 0
	global_load_lds_dwordx4 v105, s[38:39]
	s_mov_b32 m0, s30
	s_nop 0
	global_load_lds_dwordx4 v106, s[38:39]
	s_mov_b32 m0, s31
	s_nop 0
	global_load_lds_dwordx4 v107, s[38:39]
	s_mov_b32 m0, s32
	s_nop 0
	global_load_lds_dwordx4 v108, s[38:39]
	s_mov_b32 m0, s33
	s_nop 0
	global_load_lds_dwordx4 v109, s[38:39]
	s_add_u32 s36, s36, 0x80
	s_addc_u32 s37, s37, 0
	s_add_u32 s38, s38, 0x80
	s_addc_u32 s39, s39, 0
	s_waitcnt lgkmcnt(7)
	v_mfma_f32_16x16x32_f16 v[78:81], v[118:121], v[126:129], v[78:81]
	v_mfma_f32_16x16x32_f16 v[46:49], v[122:125], v[126:129], v[46:49]
	s_waitcnt lgkmcnt(6)
	v_mfma_f32_16x16x32_f16 v[74:77], v[118:121], v[130:133], v[74:77]
	v_mfma_f32_16x16x32_f16 v[42:45], v[122:125], v[130:133], v[42:45]
	s_waitcnt lgkmcnt(5)
	v_mfma_f32_16x16x32_f16 v[70:73], v[118:121], v[134:137], v[70:73]
	v_mfma_f32_16x16x32_f16 v[38:41], v[122:125], v[134:137], v[38:41]
	s_waitcnt lgkmcnt(4)
	v_mfma_f32_16x16x32_f16 v[66:69], v[118:121], v[138:141], v[66:69]
	v_mfma_f32_16x16x32_f16 v[34:37], v[122:125], v[138:141], v[34:37]
	s_waitcnt lgkmcnt(3)
	v_mfma_f32_16x16x32_f16 v[18:21], v[118:121], v[142:145], v[18:21]
	v_mfma_f32_16x16x32_f16 v[2:5], v[122:125], v[142:145], v[2:5]
	s_waitcnt lgkmcnt(2)
	v_mfma_f32_16x16x32_f16 v[26:29], v[118:121], v[146:149], v[26:29]
	v_mfma_f32_16x16x32_f16 v[10:13], v[122:125], v[146:149], v[10:13]
	s_waitcnt lgkmcnt(1)
	v_mfma_f32_16x16x32_f16 v[22:25], v[118:121], v[150:153], v[22:25]
	v_mfma_f32_16x16x32_f16 v[6:9], v[122:125], v[150:153], v[6:9]
	s_waitcnt lgkmcnt(0)
	v_mfma_f32_16x16x32_f16 v[30:33], v[118:121], v[154:157], v[30:33]
	v_mfma_f32_16x16x32_f16 v[14:17], v[122:125], v[154:157], v[14:17]
	s_waitcnt vmcnt(0)
	s_barrier
	ds_read_b128 v[110:113], v158 offset:0
	ds_read_b128 v[114:117], v158 offset:2048
	ds_read_b128 v[118:121], v159 offset:0
	ds_read_b128 v[122:125], v159 offset:2048
	ds_read_b128 v[126:129], v160 offset:16384
	ds_read_b128 v[130:133], v160 offset:18432
	ds_read_b128 v[134:137], v160 offset:20480
	ds_read_b128 v[138:141], v160 offset:22528
	ds_read_b128 v[142:145], v160 offset:24576
	ds_read_b128 v[146:149], v160 offset:26624
	ds_read_b128 v[150:153], v160 offset:28672
	ds_read_b128 v[154:157], v160 offset:30720
	s_waitcnt lgkmcnt(7)
	v_mfma_f32_16x16x32_f16 v[164:167], v[110:113], v[126:129], v[164:167]
	v_mfma_f32_16x16x32_f16 v[62:65], v[114:117], v[126:129], v[62:65]
	ds_read_b128 v[126:129], v160 offset:32768
	s_waitcnt lgkmcnt(7)
	v_mfma_f32_16x16x32_f16 v[86:89], v[110:113], v[130:133], v[86:89]
	v_mfma_f32_16x16x32_f16 v[58:61], v[114:117], v[130:133], v[58:61]
	ds_read_b128 v[130:133], v160 offset:34816
	s_waitcnt lgkmcnt(7)
	v_mfma_f32_16x16x32_f16 v[96:99], v[110:113], v[134:137], v[96:99]
	v_mfma_f32_16x16x32_f16 v[54:57], v[114:117], v[134:137], v[54:57]
	ds_read_b128 v[134:137], v160 offset:36864
	s_waitcnt lgkmcnt(7)
	v_mfma_f32_16x16x32_f16 v[82:85], v[110:113], v[138:141], v[82:85]
	v_mfma_f32_16x16x32_f16 v[50:53], v[114:117], v[138:141], v[50:53]
	ds_read_b128 v[138:141], v160 offset:38912
	s_waitcnt lgkmcnt(7)
	v_mfma_f32_16x16x32_f16 v[78:81], v[110:113], v[142:145], v[78:81]
	v_mfma_f32_16x16x32_f16 v[46:49], v[114:117], v[142:145], v[46:49]
	ds_read_b128 v[142:145], v161 offset:16384
	s_waitcnt lgkmcnt(7)
	v_mfma_f32_16x16x32_f16 v[74:77], v[110:113], v[146:149], v[74:77]
	v_mfma_f32_16x16x32_f16 v[42:45], v[114:117], v[146:149], v[42:45]
	ds_read_b128 v[146:149], v161 offset:18432
	s_waitcnt lgkmcnt(7)
	v_mfma_f32_16x16x32_f16 v[70:73], v[110:113], v[150:153], v[70:73]
	v_mfma_f32_16x16x32_f16 v[38:41], v[114:117], v[150:153], v[38:41]
	ds_read_b128 v[150:153], v161 offset:20480
	s_waitcnt lgkmcnt(7)
	v_mfma_f32_16x16x32_f16 v[66:69], v[110:113], v[154:157], v[66:69]
	v_mfma_f32_16x16x32_f16 v[34:37], v[114:117], v[154:157], v[34:37]
	ds_read_b128 v[154:157], v161 offset:22528
	s_waitcnt lgkmcnt(7)
	v_mfma_f32_16x16x32_f16 v[18:21], v[110:113], v[126:129], v[18:21]
	v_mfma_f32_16x16x32_f16 v[2:5], v[114:117], v[126:129], v[2:5]
	ds_read_b128 v[126:129], v161 offset:24576
	s_waitcnt lgkmcnt(7)
	v_mfma_f32_16x16x32_f16 v[26:29], v[110:113], v[130:133], v[26:29]
	v_mfma_f32_16x16x32_f16 v[10:13], v[114:117], v[130:133], v[10:13]
	ds_read_b128 v[130:133], v161 offset:26624
	s_waitcnt lgkmcnt(7)
	v_mfma_f32_16x16x32_f16 v[22:25], v[110:113], v[134:137], v[22:25]
	v_mfma_f32_16x16x32_f16 v[6:9], v[114:117], v[134:137], v[6:9]
	ds_read_b128 v[134:137], v161 offset:28672
	s_waitcnt lgkmcnt(7)
	v_mfma_f32_16x16x32_f16 v[30:33], v[110:113], v[138:141], v[30:33]
	v_mfma_f32_16x16x32_f16 v[14:17], v[114:117], v[138:141], v[14:17]
	ds_read_b128 v[138:141], v161 offset:30720
	s_waitcnt lgkmcnt(7)
	v_mfma_f32_16x16x32_f16 v[164:167], v[118:121], v[142:145], v[164:167]
	v_mfma_f32_16x16x32_f16 v[62:65], v[122:125], v[142:145], v[62:65]
	ds_read_b128 v[142:145], v161 offset:32768
	s_waitcnt lgkmcnt(7)
	v_mfma_f32_16x16x32_f16 v[86:89], v[118:121], v[146:149], v[86:89]
	v_mfma_f32_16x16x32_f16 v[58:61], v[122:125], v[146:149], v[58:61]
	ds_read_b128 v[146:149], v161 offset:34816
	s_waitcnt lgkmcnt(7)
	v_mfma_f32_16x16x32_f16 v[96:99], v[118:121], v[150:153], v[96:99]
	v_mfma_f32_16x16x32_f16 v[54:57], v[122:125], v[150:153], v[54:57]
	ds_read_b128 v[150:153], v161 offset:36864
	s_waitcnt lgkmcnt(7)
	v_mfma_f32_16x16x32_f16 v[82:85], v[118:121], v[154:157], v[82:85]
	v_mfma_f32_16x16x32_f16 v[50:53], v[122:125], v[154:157], v[50:53]
	ds_read_b128 v[154:157], v161 offset:38912
	s_waitcnt lgkmcnt(0)
	s_barrier
	s_mov_b32 m0, s24
	s_nop 0
	global_load_lds_dwordx4 v100, s[36:37]
	s_mov_b32 m0, s25
	s_nop 0
	global_load_lds_dwordx4 v101, s[36:37]
	s_mov_b32 m0, s26
	s_nop 0
	global_load_lds_dwordx4 v102, s[36:37]
	s_mov_b32 m0, s27
	s_nop 0
	global_load_lds_dwordx4 v103, s[36:37]
	s_mov_b32 m0, s28
	s_nop 0
	global_load_lds_dwordx4 v104, s[38:39]
	s_mov_b32 m0, s29
	s_nop 0
	global_load_lds_dwordx4 v105, s[38:39]
	s_mov_b32 m0, s30
	s_nop 0
	global_load_lds_dwordx4 v106, s[38:39]
	s_mov_b32 m0, s31
	s_nop 0
	global_load_lds_dwordx4 v107, s[38:39]
	s_mov_b32 m0, s32
	s_nop 0
	global_load_lds_dwordx4 v108, s[38:39]
	s_mov_b32 m0, s33
	s_nop 0
	global_load_lds_dwordx4 v109, s[38:39]
	s_add_u32 s36, s36, 0x80
	s_addc_u32 s37, s37, 0
	s_add_u32 s38, s38, 0x80
	s_addc_u32 s39, s39, 0
	s_waitcnt lgkmcnt(7)
	v_mfma_f32_16x16x32_f16 v[78:81], v[118:121], v[126:129], v[78:81]
	v_mfma_f32_16x16x32_f16 v[46:49], v[122:125], v[126:129], v[46:49]
	s_waitcnt lgkmcnt(6)
	v_mfma_f32_16x16x32_f16 v[74:77], v[118:121], v[130:133], v[74:77]
	v_mfma_f32_16x16x32_f16 v[42:45], v[122:125], v[130:133], v[42:45]
	s_waitcnt lgkmcnt(5)
	v_mfma_f32_16x16x32_f16 v[70:73], v[118:121], v[134:137], v[70:73]
	v_mfma_f32_16x16x32_f16 v[38:41], v[122:125], v[134:137], v[38:41]
	s_waitcnt lgkmcnt(4)
	v_mfma_f32_16x16x32_f16 v[66:69], v[118:121], v[138:141], v[66:69]
	v_mfma_f32_16x16x32_f16 v[34:37], v[122:125], v[138:141], v[34:37]
	s_waitcnt lgkmcnt(3)
	v_mfma_f32_16x16x32_f16 v[18:21], v[118:121], v[142:145], v[18:21]
	v_mfma_f32_16x16x32_f16 v[2:5], v[122:125], v[142:145], v[2:5]
	s_waitcnt lgkmcnt(2)
	v_mfma_f32_16x16x32_f16 v[26:29], v[118:121], v[146:149], v[26:29]
	v_mfma_f32_16x16x32_f16 v[10:13], v[122:125], v[146:149], v[10:13]
	s_waitcnt lgkmcnt(1)
	v_mfma_f32_16x16x32_f16 v[22:25], v[118:121], v[150:153], v[22:25]
	v_mfma_f32_16x16x32_f16 v[6:9], v[122:125], v[150:153], v[6:9]
	s_waitcnt lgkmcnt(0)
	v_mfma_f32_16x16x32_f16 v[30:33], v[118:121], v[154:157], v[30:33]
	v_mfma_f32_16x16x32_f16 v[14:17], v[122:125], v[154:157], v[14:17]
	s_waitcnt vmcnt(0)
	s_barrier
	ds_read_b128 v[110:113], v158 offset:0
	ds_read_b128 v[114:117], v158 offset:2048
	ds_read_b128 v[118:121], v159 offset:0
	ds_read_b128 v[122:125], v159 offset:2048
	ds_read_b128 v[126:129], v160 offset:16384
	ds_read_b128 v[130:133], v160 offset:18432
	ds_read_b128 v[134:137], v160 offset:20480
	ds_read_b128 v[138:141], v160 offset:22528
	ds_read_b128 v[142:145], v160 offset:24576
	ds_read_b128 v[146:149], v160 offset:26624
	ds_read_b128 v[150:153], v160 offset:28672
	ds_read_b128 v[154:157], v160 offset:30720
	s_waitcnt lgkmcnt(7)
	v_mfma_f32_16x16x32_f16 v[164:167], v[110:113], v[126:129], v[164:167]
	v_mfma_f32_16x16x32_f16 v[62:65], v[114:117], v[126:129], v[62:65]
	ds_read_b128 v[126:129], v160 offset:32768
	s_waitcnt lgkmcnt(7)
	v_mfma_f32_16x16x32_f16 v[86:89], v[110:113], v[130:133], v[86:89]
	v_mfma_f32_16x16x32_f16 v[58:61], v[114:117], v[130:133], v[58:61]
	ds_read_b128 v[130:133], v160 offset:34816
	s_waitcnt lgkmcnt(7)
	v_mfma_f32_16x16x32_f16 v[96:99], v[110:113], v[134:137], v[96:99]
	v_mfma_f32_16x16x32_f16 v[54:57], v[114:117], v[134:137], v[54:57]
	ds_read_b128 v[134:137], v160 offset:36864
	s_waitcnt lgkmcnt(7)
	v_mfma_f32_16x16x32_f16 v[82:85], v[110:113], v[138:141], v[82:85]
	v_mfma_f32_16x16x32_f16 v[50:53], v[114:117], v[138:141], v[50:53]
	ds_read_b128 v[138:141], v160 offset:38912
	s_waitcnt lgkmcnt(7)
	v_mfma_f32_16x16x32_f16 v[78:81], v[110:113], v[142:145], v[78:81]
	v_mfma_f32_16x16x32_f16 v[46:49], v[114:117], v[142:145], v[46:49]
	ds_read_b128 v[142:145], v161 offset:16384
	s_waitcnt lgkmcnt(7)
	v_mfma_f32_16x16x32_f16 v[74:77], v[110:113], v[146:149], v[74:77]
	v_mfma_f32_16x16x32_f16 v[42:45], v[114:117], v[146:149], v[42:45]
	ds_read_b128 v[146:149], v161 offset:18432
	s_waitcnt lgkmcnt(7)
	v_mfma_f32_16x16x32_f16 v[70:73], v[110:113], v[150:153], v[70:73]
	v_mfma_f32_16x16x32_f16 v[38:41], v[114:117], v[150:153], v[38:41]
	ds_read_b128 v[150:153], v161 offset:20480
	s_waitcnt lgkmcnt(7)
	v_mfma_f32_16x16x32_f16 v[66:69], v[110:113], v[154:157], v[66:69]
	v_mfma_f32_16x16x32_f16 v[34:37], v[114:117], v[154:157], v[34:37]
	ds_read_b128 v[154:157], v161 offset:22528
	s_waitcnt lgkmcnt(7)
	v_mfma_f32_16x16x32_f16 v[18:21], v[110:113], v[126:129], v[18:21]
	v_mfma_f32_16x16x32_f16 v[2:5], v[114:117], v[126:129], v[2:5]
	ds_read_b128 v[126:129], v161 offset:24576
	s_waitcnt lgkmcnt(7)
	v_mfma_f32_16x16x32_f16 v[26:29], v[110:113], v[130:133], v[26:29]
	v_mfma_f32_16x16x32_f16 v[10:13], v[114:117], v[130:133], v[10:13]
	ds_read_b128 v[130:133], v161 offset:26624
	s_waitcnt lgkmcnt(7)
	v_mfma_f32_16x16x32_f16 v[22:25], v[110:113], v[134:137], v[22:25]
	v_mfma_f32_16x16x32_f16 v[6:9], v[114:117], v[134:137], v[6:9]
	ds_read_b128 v[134:137], v161 offset:28672
	s_waitcnt lgkmcnt(7)
	v_mfma_f32_16x16x32_f16 v[30:33], v[110:113], v[138:141], v[30:33]
	v_mfma_f32_16x16x32_f16 v[14:17], v[114:117], v[138:141], v[14:17]
	ds_read_b128 v[138:141], v161 offset:30720
	s_waitcnt lgkmcnt(7)
	v_mfma_f32_16x16x32_f16 v[164:167], v[118:121], v[142:145], v[164:167]
	v_mfma_f32_16x16x32_f16 v[62:65], v[122:125], v[142:145], v[62:65]
	ds_read_b128 v[142:145], v161 offset:32768
	s_waitcnt lgkmcnt(7)
	v_mfma_f32_16x16x32_f16 v[86:89], v[118:121], v[146:149], v[86:89]
	v_mfma_f32_16x16x32_f16 v[58:61], v[122:125], v[146:149], v[58:61]
	ds_read_b128 v[146:149], v161 offset:34816
	s_waitcnt lgkmcnt(7)
	v_mfma_f32_16x16x32_f16 v[96:99], v[118:121], v[150:153], v[96:99]
	v_mfma_f32_16x16x32_f16 v[54:57], v[122:125], v[150:153], v[54:57]
	ds_read_b128 v[150:153], v161 offset:36864
	s_waitcnt lgkmcnt(7)
	v_mfma_f32_16x16x32_f16 v[82:85], v[118:121], v[154:157], v[82:85]
	v_mfma_f32_16x16x32_f16 v[50:53], v[122:125], v[154:157], v[50:53]
	ds_read_b128 v[154:157], v161 offset:38912
	s_waitcnt lgkmcnt(0)
	s_barrier
	s_mov_b32 m0, s24
	s_nop 0
	global_load_lds_dwordx4 v100, s[36:37]
	s_mov_b32 m0, s25
	s_nop 0
	global_load_lds_dwordx4 v101, s[36:37]
	s_mov_b32 m0, s26
	s_nop 0
	global_load_lds_dwordx4 v102, s[36:37]
	s_mov_b32 m0, s27
	s_nop 0
	global_load_lds_dwordx4 v103, s[36:37]
	s_mov_b32 m0, s28
	s_nop 0
	global_load_lds_dwordx4 v104, s[38:39]
	s_mov_b32 m0, s29
	s_nop 0
	global_load_lds_dwordx4 v105, s[38:39]
	s_mov_b32 m0, s30
	s_nop 0
	global_load_lds_dwordx4 v106, s[38:39]
	s_mov_b32 m0, s31
	s_nop 0
	global_load_lds_dwordx4 v107, s[38:39]
	s_mov_b32 m0, s32
	s_nop 0
	global_load_lds_dwordx4 v108, s[38:39]
	s_mov_b32 m0, s33
	s_nop 0
	global_load_lds_dwordx4 v109, s[38:39]
	s_add_u32 s36, s36, 0x80
	s_addc_u32 s37, s37, 0
	s_add_u32 s38, s38, 0x80
	s_addc_u32 s39, s39, 0
	s_waitcnt lgkmcnt(7)
	v_mfma_f32_16x16x32_f16 v[78:81], v[118:121], v[126:129], v[78:81]
	v_mfma_f32_16x16x32_f16 v[46:49], v[122:125], v[126:129], v[46:49]
	s_waitcnt lgkmcnt(6)
	v_mfma_f32_16x16x32_f16 v[74:77], v[118:121], v[130:133], v[74:77]
	v_mfma_f32_16x16x32_f16 v[42:45], v[122:125], v[130:133], v[42:45]
	s_waitcnt lgkmcnt(5)
	v_mfma_f32_16x16x32_f16 v[70:73], v[118:121], v[134:137], v[70:73]
	v_mfma_f32_16x16x32_f16 v[38:41], v[122:125], v[134:137], v[38:41]
	s_waitcnt lgkmcnt(4)
	v_mfma_f32_16x16x32_f16 v[66:69], v[118:121], v[138:141], v[66:69]
	v_mfma_f32_16x16x32_f16 v[34:37], v[122:125], v[138:141], v[34:37]
	s_waitcnt lgkmcnt(3)
	v_mfma_f32_16x16x32_f16 v[18:21], v[118:121], v[142:145], v[18:21]
	v_mfma_f32_16x16x32_f16 v[2:5], v[122:125], v[142:145], v[2:5]
	s_waitcnt lgkmcnt(2)
	v_mfma_f32_16x16x32_f16 v[26:29], v[118:121], v[146:149], v[26:29]
	v_mfma_f32_16x16x32_f16 v[10:13], v[122:125], v[146:149], v[10:13]
	s_waitcnt lgkmcnt(1)
	v_mfma_f32_16x16x32_f16 v[22:25], v[118:121], v[150:153], v[22:25]
	v_mfma_f32_16x16x32_f16 v[6:9], v[122:125], v[150:153], v[6:9]
	s_waitcnt lgkmcnt(0)
	v_mfma_f32_16x16x32_f16 v[30:33], v[118:121], v[154:157], v[30:33]
	v_mfma_f32_16x16x32_f16 v[14:17], v[122:125], v[154:157], v[14:17]
	s_waitcnt vmcnt(0)
	s_barrier
	ds_read_b128 v[110:113], v158 offset:0
	ds_read_b128 v[114:117], v158 offset:2048
	ds_read_b128 v[118:121], v159 offset:0
	ds_read_b128 v[122:125], v159 offset:2048
	ds_read_b128 v[126:129], v160 offset:16384
	ds_read_b128 v[130:133], v160 offset:18432
	ds_read_b128 v[134:137], v160 offset:20480
	ds_read_b128 v[138:141], v160 offset:22528
	ds_read_b128 v[142:145], v160 offset:24576
	ds_read_b128 v[146:149], v160 offset:26624
	ds_read_b128 v[150:153], v160 offset:28672
	ds_read_b128 v[154:157], v160 offset:30720
	s_waitcnt lgkmcnt(7)
	v_mfma_f32_16x16x32_f16 v[164:167], v[110:113], v[126:129], v[164:167]
	v_mfma_f32_16x16x32_f16 v[62:65], v[114:117], v[126:129], v[62:65]
	ds_read_b128 v[126:129], v160 offset:32768
	s_waitcnt lgkmcnt(7)
	v_mfma_f32_16x16x32_f16 v[86:89], v[110:113], v[130:133], v[86:89]
	v_mfma_f32_16x16x32_f16 v[58:61], v[114:117], v[130:133], v[58:61]
	ds_read_b128 v[130:133], v160 offset:34816
	s_waitcnt lgkmcnt(7)
	v_mfma_f32_16x16x32_f16 v[96:99], v[110:113], v[134:137], v[96:99]
	v_mfma_f32_16x16x32_f16 v[54:57], v[114:117], v[134:137], v[54:57]
	ds_read_b128 v[134:137], v160 offset:36864
	s_waitcnt lgkmcnt(7)
	v_mfma_f32_16x16x32_f16 v[82:85], v[110:113], v[138:141], v[82:85]
	v_mfma_f32_16x16x32_f16 v[50:53], v[114:117], v[138:141], v[50:53]
	ds_read_b128 v[138:141], v160 offset:38912
	s_waitcnt lgkmcnt(7)
	v_mfma_f32_16x16x32_f16 v[78:81], v[110:113], v[142:145], v[78:81]
	v_mfma_f32_16x16x32_f16 v[46:49], v[114:117], v[142:145], v[46:49]
	ds_read_b128 v[142:145], v161 offset:16384
	s_waitcnt lgkmcnt(7)
	v_mfma_f32_16x16x32_f16 v[74:77], v[110:113], v[146:149], v[74:77]
	v_mfma_f32_16x16x32_f16 v[42:45], v[114:117], v[146:149], v[42:45]
	ds_read_b128 v[146:149], v161 offset:18432
	s_waitcnt lgkmcnt(7)
	v_mfma_f32_16x16x32_f16 v[70:73], v[110:113], v[150:153], v[70:73]
	v_mfma_f32_16x16x32_f16 v[38:41], v[114:117], v[150:153], v[38:41]
	ds_read_b128 v[150:153], v161 offset:20480
	s_waitcnt lgkmcnt(7)
	v_mfma_f32_16x16x32_f16 v[66:69], v[110:113], v[154:157], v[66:69]
	v_mfma_f32_16x16x32_f16 v[34:37], v[114:117], v[154:157], v[34:37]
	ds_read_b128 v[154:157], v161 offset:22528
	s_waitcnt lgkmcnt(7)
	v_mfma_f32_16x16x32_f16 v[18:21], v[110:113], v[126:129], v[18:21]
	v_mfma_f32_16x16x32_f16 v[2:5], v[114:117], v[126:129], v[2:5]
	ds_read_b128 v[126:129], v161 offset:24576
	s_waitcnt lgkmcnt(7)
	v_mfma_f32_16x16x32_f16 v[26:29], v[110:113], v[130:133], v[26:29]
	v_mfma_f32_16x16x32_f16 v[10:13], v[114:117], v[130:133], v[10:13]
	ds_read_b128 v[130:133], v161 offset:26624
	s_waitcnt lgkmcnt(7)
	v_mfma_f32_16x16x32_f16 v[22:25], v[110:113], v[134:137], v[22:25]
	v_mfma_f32_16x16x32_f16 v[6:9], v[114:117], v[134:137], v[6:9]
	ds_read_b128 v[134:137], v161 offset:28672
	s_waitcnt lgkmcnt(7)
	v_mfma_f32_16x16x32_f16 v[30:33], v[110:113], v[138:141], v[30:33]
	v_mfma_f32_16x16x32_f16 v[14:17], v[114:117], v[138:141], v[14:17]
	ds_read_b128 v[138:141], v161 offset:30720
	s_waitcnt lgkmcnt(7)
	v_mfma_f32_16x16x32_f16 v[164:167], v[118:121], v[142:145], v[164:167]
	v_mfma_f32_16x16x32_f16 v[62:65], v[122:125], v[142:145], v[62:65]
	ds_read_b128 v[142:145], v161 offset:32768
	s_waitcnt lgkmcnt(7)
	v_mfma_f32_16x16x32_f16 v[86:89], v[118:121], v[146:149], v[86:89]
	v_mfma_f32_16x16x32_f16 v[58:61], v[122:125], v[146:149], v[58:61]
	ds_read_b128 v[146:149], v161 offset:34816
	s_waitcnt lgkmcnt(7)
	v_mfma_f32_16x16x32_f16 v[96:99], v[118:121], v[150:153], v[96:99]
	v_mfma_f32_16x16x32_f16 v[54:57], v[122:125], v[150:153], v[54:57]
	ds_read_b128 v[150:153], v161 offset:36864
	s_waitcnt lgkmcnt(7)
	v_mfma_f32_16x16x32_f16 v[82:85], v[118:121], v[154:157], v[82:85]
	v_mfma_f32_16x16x32_f16 v[50:53], v[122:125], v[154:157], v[50:53]
	ds_read_b128 v[154:157], v161 offset:38912
	s_waitcnt lgkmcnt(0)
	s_barrier
	s_mov_b32 m0, s24
	s_nop 0
	global_load_lds_dwordx4 v100, s[36:37]
	s_mov_b32 m0, s25
	s_nop 0
	global_load_lds_dwordx4 v101, s[36:37]
	s_mov_b32 m0, s26
	s_nop 0
	global_load_lds_dwordx4 v102, s[36:37]
	s_mov_b32 m0, s27
	s_nop 0
	global_load_lds_dwordx4 v103, s[36:37]
	s_mov_b32 m0, s28
	s_nop 0
	global_load_lds_dwordx4 v104, s[38:39]
	s_mov_b32 m0, s29
	s_nop 0
	global_load_lds_dwordx4 v105, s[38:39]
	s_mov_b32 m0, s30
	s_nop 0
	global_load_lds_dwordx4 v106, s[38:39]
	s_mov_b32 m0, s31
	s_nop 0
	global_load_lds_dwordx4 v107, s[38:39]
	s_mov_b32 m0, s32
	s_nop 0
	global_load_lds_dwordx4 v108, s[38:39]
	s_mov_b32 m0, s33
	s_nop 0
	global_load_lds_dwordx4 v109, s[38:39]
	s_add_u32 s36, s36, 0x80
	s_addc_u32 s37, s37, 0
	s_add_u32 s38, s38, 0x80
	s_addc_u32 s39, s39, 0
	s_waitcnt lgkmcnt(7)
	v_mfma_f32_16x16x32_f16 v[78:81], v[118:121], v[126:129], v[78:81]
	v_mfma_f32_16x16x32_f16 v[46:49], v[122:125], v[126:129], v[46:49]
	s_waitcnt lgkmcnt(6)
	v_mfma_f32_16x16x32_f16 v[74:77], v[118:121], v[130:133], v[74:77]
	v_mfma_f32_16x16x32_f16 v[42:45], v[122:125], v[130:133], v[42:45]
	s_waitcnt lgkmcnt(5)
	v_mfma_f32_16x16x32_f16 v[70:73], v[118:121], v[134:137], v[70:73]
	v_mfma_f32_16x16x32_f16 v[38:41], v[122:125], v[134:137], v[38:41]
	s_waitcnt lgkmcnt(4)
	v_mfma_f32_16x16x32_f16 v[66:69], v[118:121], v[138:141], v[66:69]
	v_mfma_f32_16x16x32_f16 v[34:37], v[122:125], v[138:141], v[34:37]
	s_waitcnt lgkmcnt(3)
	v_mfma_f32_16x16x32_f16 v[18:21], v[118:121], v[142:145], v[18:21]
	v_mfma_f32_16x16x32_f16 v[2:5], v[122:125], v[142:145], v[2:5]
	s_waitcnt lgkmcnt(2)
	v_mfma_f32_16x16x32_f16 v[26:29], v[118:121], v[146:149], v[26:29]
	v_mfma_f32_16x16x32_f16 v[10:13], v[122:125], v[146:149], v[10:13]
	s_waitcnt lgkmcnt(1)
	v_mfma_f32_16x16x32_f16 v[22:25], v[118:121], v[150:153], v[22:25]
	v_mfma_f32_16x16x32_f16 v[6:9], v[122:125], v[150:153], v[6:9]
	s_waitcnt lgkmcnt(0)
	v_mfma_f32_16x16x32_f16 v[30:33], v[118:121], v[154:157], v[30:33]
	v_mfma_f32_16x16x32_f16 v[14:17], v[122:125], v[154:157], v[14:17]
	s_waitcnt vmcnt(0)
	s_barrier
	ds_read_b128 v[110:113], v158 offset:0
	ds_read_b128 v[114:117], v158 offset:2048
	ds_read_b128 v[118:121], v159 offset:0
	ds_read_b128 v[122:125], v159 offset:2048
	ds_read_b128 v[126:129], v160 offset:16384
	ds_read_b128 v[130:133], v160 offset:18432
	ds_read_b128 v[134:137], v160 offset:20480
	ds_read_b128 v[138:141], v160 offset:22528
	ds_read_b128 v[142:145], v160 offset:24576
	ds_read_b128 v[146:149], v160 offset:26624
	ds_read_b128 v[150:153], v160 offset:28672
	ds_read_b128 v[154:157], v160 offset:30720
	s_waitcnt lgkmcnt(7)
	v_mfma_f32_16x16x32_f16 v[164:167], v[110:113], v[126:129], v[164:167]
	v_mfma_f32_16x16x32_f16 v[62:65], v[114:117], v[126:129], v[62:65]
	ds_read_b128 v[126:129], v160 offset:32768
	s_waitcnt lgkmcnt(7)
	v_mfma_f32_16x16x32_f16 v[86:89], v[110:113], v[130:133], v[86:89]
	v_mfma_f32_16x16x32_f16 v[58:61], v[114:117], v[130:133], v[58:61]
	ds_read_b128 v[130:133], v160 offset:34816
	s_waitcnt lgkmcnt(7)
	v_mfma_f32_16x16x32_f16 v[96:99], v[110:113], v[134:137], v[96:99]
	v_mfma_f32_16x16x32_f16 v[54:57], v[114:117], v[134:137], v[54:57]
	ds_read_b128 v[134:137], v160 offset:36864
	s_waitcnt lgkmcnt(7)
	v_mfma_f32_16x16x32_f16 v[82:85], v[110:113], v[138:141], v[82:85]
	v_mfma_f32_16x16x32_f16 v[50:53], v[114:117], v[138:141], v[50:53]
	ds_read_b128 v[138:141], v160 offset:38912
	s_waitcnt lgkmcnt(7)
	v_mfma_f32_16x16x32_f16 v[78:81], v[110:113], v[142:145], v[78:81]
	v_mfma_f32_16x16x32_f16 v[46:49], v[114:117], v[142:145], v[46:49]
	ds_read_b128 v[142:145], v161 offset:16384
	s_waitcnt lgkmcnt(7)
	v_mfma_f32_16x16x32_f16 v[74:77], v[110:113], v[146:149], v[74:77]
	v_mfma_f32_16x16x32_f16 v[42:45], v[114:117], v[146:149], v[42:45]
	ds_read_b128 v[146:149], v161 offset:18432
	s_waitcnt lgkmcnt(7)
	v_mfma_f32_16x16x32_f16 v[70:73], v[110:113], v[150:153], v[70:73]
	v_mfma_f32_16x16x32_f16 v[38:41], v[114:117], v[150:153], v[38:41]
	ds_read_b128 v[150:153], v161 offset:20480
	s_waitcnt lgkmcnt(7)
	v_mfma_f32_16x16x32_f16 v[66:69], v[110:113], v[154:157], v[66:69]
	v_mfma_f32_16x16x32_f16 v[34:37], v[114:117], v[154:157], v[34:37]
	ds_read_b128 v[154:157], v161 offset:22528
	s_waitcnt lgkmcnt(7)
	v_mfma_f32_16x16x32_f16 v[18:21], v[110:113], v[126:129], v[18:21]
	v_mfma_f32_16x16x32_f16 v[2:5], v[114:117], v[126:129], v[2:5]
	ds_read_b128 v[126:129], v161 offset:24576
	s_waitcnt lgkmcnt(7)
	v_mfma_f32_16x16x32_f16 v[26:29], v[110:113], v[130:133], v[26:29]
	v_mfma_f32_16x16x32_f16 v[10:13], v[114:117], v[130:133], v[10:13]
	ds_read_b128 v[130:133], v161 offset:26624
	s_waitcnt lgkmcnt(7)
	v_mfma_f32_16x16x32_f16 v[22:25], v[110:113], v[134:137], v[22:25]
	v_mfma_f32_16x16x32_f16 v[6:9], v[114:117], v[134:137], v[6:9]
	ds_read_b128 v[134:137], v161 offset:28672
	s_waitcnt lgkmcnt(7)
	v_mfma_f32_16x16x32_f16 v[30:33], v[110:113], v[138:141], v[30:33]
	v_mfma_f32_16x16x32_f16 v[14:17], v[114:117], v[138:141], v[14:17]
	ds_read_b128 v[138:141], v161 offset:30720
	s_waitcnt lgkmcnt(7)
	v_mfma_f32_16x16x32_f16 v[164:167], v[118:121], v[142:145], v[164:167]
	v_mfma_f32_16x16x32_f16 v[62:65], v[122:125], v[142:145], v[62:65]
	ds_read_b128 v[142:145], v161 offset:32768
	s_waitcnt lgkmcnt(7)
	v_mfma_f32_16x16x32_f16 v[86:89], v[118:121], v[146:149], v[86:89]
	v_mfma_f32_16x16x32_f16 v[58:61], v[122:125], v[146:149], v[58:61]
	ds_read_b128 v[146:149], v161 offset:34816
	s_waitcnt lgkmcnt(7)
	v_mfma_f32_16x16x32_f16 v[96:99], v[118:121], v[150:153], v[96:99]
	v_mfma_f32_16x16x32_f16 v[54:57], v[122:125], v[150:153], v[54:57]
	ds_read_b128 v[150:153], v161 offset:36864
	s_waitcnt lgkmcnt(7)
	v_mfma_f32_16x16x32_f16 v[82:85], v[118:121], v[154:157], v[82:85]
	v_mfma_f32_16x16x32_f16 v[50:53], v[122:125], v[154:157], v[50:53]
	ds_read_b128 v[154:157], v161 offset:38912
	s_waitcnt lgkmcnt(0)
	s_barrier
	s_waitcnt lgkmcnt(7)
	v_mfma_f32_16x16x32_f16 v[78:81], v[118:121], v[126:129], v[78:81]
	v_mfma_f32_16x16x32_f16 v[46:49], v[122:125], v[126:129], v[46:49]
	s_waitcnt lgkmcnt(6)
	v_mfma_f32_16x16x32_f16 v[74:77], v[118:121], v[130:133], v[74:77]
	v_mfma_f32_16x16x32_f16 v[42:45], v[122:125], v[130:133], v[42:45]
	s_waitcnt lgkmcnt(5)
	v_mfma_f32_16x16x32_f16 v[70:73], v[118:121], v[134:137], v[70:73]
	v_mfma_f32_16x16x32_f16 v[38:41], v[122:125], v[134:137], v[38:41]
	s_waitcnt lgkmcnt(4)
	v_mfma_f32_16x16x32_f16 v[66:69], v[118:121], v[138:141], v[66:69]
	v_mfma_f32_16x16x32_f16 v[34:37], v[122:125], v[138:141], v[34:37]
	s_waitcnt lgkmcnt(3)
	v_mfma_f32_16x16x32_f16 v[18:21], v[118:121], v[142:145], v[18:21]
	v_mfma_f32_16x16x32_f16 v[2:5], v[122:125], v[142:145], v[2:5]
	s_waitcnt lgkmcnt(2)
	v_mfma_f32_16x16x32_f16 v[26:29], v[118:121], v[146:149], v[26:29]
	v_mfma_f32_16x16x32_f16 v[10:13], v[122:125], v[146:149], v[10:13]
	s_waitcnt lgkmcnt(1)
	v_mfma_f32_16x16x32_f16 v[22:25], v[118:121], v[150:153], v[22:25]
	v_mfma_f32_16x16x32_f16 v[6:9], v[122:125], v[150:153], v[6:9]
	s_waitcnt lgkmcnt(0)
	v_mfma_f32_16x16x32_f16 v[30:33], v[118:121], v[154:157], v[30:33]
	v_mfma_f32_16x16x32_f16 v[14:17], v[122:125], v[154:157], v[14:17]
	s_nop 15
	s_nop 15
	s_movk_i32 s2, 0xfc
	v_cmp_gt_u32_e32 vcc, s2, v0
	s_mov_b32 s2, 0x12492493
	s_movk_i32 s4, 0x380
	s_movk_i32 s12, 0x110
	v_cmp_gt_u32_e64 s[4:5], s4, v0
	v_lshrrev_b32_e32 v93, 1, v0
	v_cndmask_b32_e32 v94, 0, v93, vcc
	s_nop 5
	v_cvt_f16_f32_e32 v86, v86
	s_nop 5
	v_cvt_f16_f32_e32 v54, v54
	v_cvt_f16_f32_e32 v82, v82
	v_cvt_f16_f32_e32 v50, v50
	s_nop 5
	v_cvt_f16_f32_e32 v78, v78
	v_mul_i32_i24_e32 v102, 0xffffffc2, v92
	v_mul_u32_u24_e32 v101, 0x110, v91
	v_lshlrev_b32_e32 v91, 6, v92
	v_add3_u32 v91, v91, v102, v101
	ds_write_b16 v91, v86 offset:32
	v_cvt_f16_f32_e32 v86, v87
	v_cvt_f16_f32_e32 v74, v74
	v_cvt_f16_f32_e32 v102, v165
	ds_write_b16 v91, v86 offset:304
	v_cvt_f16_f32_e32 v86, v88
	s_nop 2
	v_cvt_f16_f32_e32 v34, v34
	ds_write_b16 v91, v82 offset:96
	ds_write_b16 v91, v86 offset:576
	v_cvt_f16_f32_e32 v86, v89
	v_cvt_f16_f32_e32 v38, v38
	ds_write_b16 v91, v34 offset:4576
	ds_write_b16 v91, v86 offset:848
	v_cvt_f16_f32_e32 v86, v96
	s_nop 1
	v_cvt_f16_f32_e32 v62, v62
	v_cvt_f16_f32_e32 v34, v35
	s_nop 0
	v_cvt_f16_f32_e32 v58, v58
	ds_write_b16 v91, v38 offset:4544
	v_cvt_f16_f32_e32 v38, v39
	s_nop 1
	v_cvt_f16_f32_e32 v46, v46
	ds_write_b16 v91, v86 offset:64
	v_cvt_f16_f32_e32 v86, v97
	s_nop 0
	v_cvt_f16_f32_e32 v42, v42
	v_cvt_f16_f32_e32 v82, v83
	ds_write_b16 v91, v78 offset:128
	s_nop 1
	v_cvt_f16_f32_e32 v70, v70
	v_cvt_f16_f32_e32 v78, v79
	ds_write_b16 v91, v74 offset:160
	v_cvt_f16_f32_e32 v74, v75
	s_nop 0
	v_cvt_f16_f32_e32 v66, v66
	ds_write_b16 v91, v70 offset:192
	v_cvt_f16_f32_e32 v70, v71
	ds_write_b16 v91, v62 offset:4352
	ds_write_b16 v91, v66 offset:224
	v_cvt_f16_f32_e32 v66, v67
	v_cvt_f16_f32_e32 v62, v63
	ds_write_b16 v91, v58 offset:4384
	v_cvt_f16_f32_e32 v58, v59
	ds_write_b16 v91, v54 offset:4416
	v_cvt_f16_f32_e32 v54, v55
	ds_write_b16 v91, v50 offset:4448
	v_cvt_f16_f32_e32 v50, v51
	ds_write_b16 v91, v46 offset:4480
	v_cvt_f16_f32_e32 v46, v47
	ds_write_b16 v91, v42 offset:4512
	v_cvt_f16_f32_e32 v42, v43
	ds_write_b16 v91, v34 offset:4848
	v_cvt_f16_f32_e32 v34, v36
	ds_write_b16 v91, v38 offset:4816
	v_cvt_f16_f32_e32 v38, v40
	ds_write_b16 v91, v102 offset:272
	v_cvt_f16_f32_e32 v102, v166
	ds_write_b16 v91, v86 offset:336
	v_cvt_f16_f32_e32 v86, v98
	ds_write_b16 v91, v82 offset:368
	v_cvt_f16_f32_e32 v82, v84
	ds_write_b16 v91, v78 offset:400
	v_cvt_f16_f32_e32 v78, v80
	ds_write_b16 v91, v74 offset:432
	v_cvt_f16_f32_e32 v74, v76
	ds_write_b16 v91, v70 offset:464
	v_cvt_f16_f32_e32 v70, v72
	ds_write_b16 v91, v66 offset:496
	v_cvt_f16_f32_e32 v66, v68
	ds_write_b16 v91, v62 offset:4624
	v_cvt_f16_f32_e32 v62, v64
	ds_write_b16 v91, v58 offset:4656
	v_cvt_f16_f32_e32 v58, v60
	ds_write_b16 v91, v54 offset:4688
	v_cvt_f16_f32_e32 v54, v56
	ds_write_b16 v91, v50 offset:4720
	v_cvt_f16_f32_e32 v50, v52
	ds_write_b16 v91, v46 offset:4752
	v_cvt_f16_f32_e32 v46, v48
	ds_write_b16 v91, v42 offset:4784
	v_cvt_f16_f32_e32 v42, v44
	ds_write_b16 v91, v34 offset:5120
	v_cvt_f16_f32_e32 v34, v37
	ds_write_b16 v91, v38 offset:5088
	v_cvt_f16_f32_e32 v38, v41
	v_cvt_f16_f32_e32 v103, v164
	ds_write_b16 v91, v102 offset:544
	v_cvt_f16_f32_e32 v102, v167
	ds_write_b16 v91, v86 offset:608
	v_cvt_f16_f32_e32 v86, v99
	ds_write_b16 v91, v82 offset:640
	v_cvt_f16_f32_e32 v82, v85
	ds_write_b16 v91, v78 offset:672
	v_cvt_f16_f32_e32 v78, v81
	ds_write_b16 v91, v74 offset:704
	v_cvt_f16_f32_e32 v74, v77
	ds_write_b16 v91, v70 offset:736
	v_cvt_f16_f32_e32 v70, v73
	ds_write_b16 v91, v66 offset:768
	v_cvt_f16_f32_e32 v66, v69
	ds_write_b16 v91, v62 offset:4896
	v_cvt_f16_f32_e32 v62, v65
	ds_write_b16 v91, v58 offset:4928
	v_cvt_f16_f32_e32 v58, v61
	ds_write_b16 v91, v54 offset:4960
	v_cvt_f16_f32_e32 v54, v57
	ds_write_b16 v91, v50 offset:4992
	v_cvt_f16_f32_e32 v50, v53
	ds_write_b16 v91, v46 offset:5024
	v_cvt_f16_f32_e32 v46, v49
	ds_write_b16 v91, v42 offset:5056
	v_cvt_f16_f32_e32 v42, v45
	ds_write_b16 v91, v34 offset:5392
	v_min_u32_e32 v34, 8, v92
	v_mul_hi_u32 v100, v94, s2
	ds_write_b16 v91, v38 offset:5360
	v_cmp_gt_u32_e64 s[2:3], 9, v92
	v_mul_u32_u24_e32 v39, 14, v34
	v_and_b32_e32 v40, 48, v0
	v_lshlrev_b32_e32 v38, 2, v92
	ds_write_b16 v91, v103
	ds_write_b16 v91, v102 offset:816
	ds_write_b16 v91, v86 offset:880
	ds_write_b16 v91, v82 offset:912
	ds_write_b16 v91, v78 offset:944
	ds_write_b16 v91, v74 offset:976
	ds_write_b16 v91, v70 offset:1008
	ds_write_b16 v91, v66 offset:1040
	ds_write_b16 v91, v62 offset:5168
	ds_write_b16 v91, v58 offset:5200
	ds_write_b16 v91, v54 offset:5232
	ds_write_b16 v91, v50 offset:5264
	ds_write_b16 v91, v46 offset:5296
	ds_write_b16 v91, v42 offset:5328
	s_waitcnt lgkmcnt(0)
	s_barrier
	s_and_saveexec_b64 s[6:7], s[4:5]
	s_cbranch_execz .LBB1_9
	v_add_u32_e32 v34, v1, v39
	v_mad_u32_u24 v41, v34, s12, v40
	ds_read_b128 v[34:37], v41
	ds_read_b128 v[42:45], v41 offset:64
	ds_read_b128 v[46:49], v41 offset:128
	ds_read_b128 v[50:53], v41 offset:192
	v_cmp_ne_u32_e64 s[4:5], 3, v90
	v_mul_u32_u24_e32 v41, 9, v1
	s_and_b64 s[12:13], s[4:5], s[2:3]
	s_waitcnt lgkmcnt(1)
	v_mfma_f32_16x16x32_f16 v[34:37], v[34:37], v[46:49], 0
	s_waitcnt lgkmcnt(0)
	v_mfma_f32_16x16x32_f16 v[34:37], v[42:45], v[50:53], v[34:37]
	s_and_saveexec_b64 s[4:5], s[12:13]
	v_add_u32_e32 v42, v95, v41
	s_nop 5
	v_mul_f32_e32 v34, 0x3e000000, v34
	v_mad_u32_u24 v42, v42, 48, v38
	ds_write_b32 v42, v34 offset:35328
	s_or_b64 exec, exec, s[4:5]
	v_or_b32_e32 v34, 1, v95
	v_cmp_gt_u32_e64 s[4:5], 9, v34
	s_and_b64 s[12:13], s[4:5], s[2:3]
	s_and_saveexec_b64 s[4:5], s[12:13]
	v_add_u32_e32 v34, v34, v41
	v_mul_f32_e32 v35, 0x3e000000, v35
	v_mad_u32_u24 v34, v34, 48, v38
	ds_write_b32 v34, v35 offset:35328
	s_or_b64 exec, exec, s[4:5]
	v_or_b32_e32 v34, 2, v95
	v_cmp_gt_u32_e64 s[4:5], 9, v34
	s_and_b64 s[12:13], s[4:5], s[2:3]
	s_and_saveexec_b64 s[4:5], s[12:13]
	v_add_u32_e32 v34, v34, v41
	v_mul_f32_e32 v35, 0x3e000000, v36
	v_mad_u32_u24 v34, v34, 48, v38
	ds_write_b32 v34, v35 offset:35328
	s_or_b64 exec, exec, s[4:5]
	v_or_b32_e32 v34, 3, v95
	v_cmp_gt_u32_e64 s[4:5], 9, v34
	s_and_b64 s[4:5], s[4:5], s[2:3]
	s_and_b64 exec, exec, s[4:5]
	v_add_u32_e32 v34, v34, v41
	v_mul_f32_e32 v35, 0x3e000000, v37
	v_mad_u32_u24 v34, v34, 48, v38
	ds_write_b32 v34, v35 offset:35328

_Z9k_spatialPKDF16_S0_S0_PfPDF16_:
	s_load_dwordx4 s[4:7], s[0:1], 0x0
	s_load_dwordx2 s[10:11], s[0:1], 0x10
	s_mul_hi_i32 s9, s2, 0x3140
	s_mul_i32 s8, s2, 0x3140
	s_lshl_b64 s[8:9], s[8:9], 1
	v_and_b32_e32 v2, 7, v0
	v_lshrrev_b32_e32 v3, 3, v0
	v_lshlrev_b32_e32 v10, 4, v2
	v_lshl_or_b32 v4, v3, 7, v10
	v_add_u32_e32 v5, 0x1c00, v4
	v_add_u32_e32 v6, 0x3800, v4
	v_add_u32_e32 v7, 0x5400, v4
	v_lshrrev_b32_e32 v8, 1, v0
	v_and_b32_e32 v108, 31, v0
	v_and_b32_e32 v115, 0xe0, v8
	v_or_b32_e32 v109, v115, v108
	s_movk_i32 s3, 0xc5
	v_mov_b32_e32 v8, 0xc4
	v_cmp_gt_u32_e64 s[12:13], s3, v109
	v_bfe_u32 v1, v0, 5, 1
	v_lshlrev_b32_e32 v111, 4, v1
	s_nop 1
	v_cndmask_b32_e64 v110, v8, v109, s[12:13]
	v_lshl_or_b32 v9, v110, 7, v111
	s_movk_i32 s3, 0xe8
	v_cmp_gt_u32_e32 vcc, s3, v0
	v_or_b32_e32 v14, 0x6200, v10
	s_nop 1
	v_cndmask_b32_e32 v7, v14, v7, vcc
	s_waitcnt lgkmcnt(0)
	s_add_u32 s6, s6, s8
	s_addc_u32 s7, s7, s9
	s_add_u32 s10, s10, s8
	s_addc_u32 s11, s11, s9
	s_add_u32 s4, s4, s8
	s_addc_u32 s5, s5, s9
	global_load_dwordx4 v[18:21], v4, s[6:7] nt
	global_load_dwordx4 v[22:25], v4, s[10:11] nt
	global_load_dwordx4 v[26:29], v5, s[6:7] nt
	global_load_dwordx4 v[30:33], v5, s[10:11] nt
	global_load_dwordx4 v[34:37], v6, s[6:7] nt
	global_load_dwordx4 v[38:41], v6, s[10:11] nt
	global_load_dwordx4 v[42:45], v7, s[6:7] nt
	global_load_dwordx4 v[46:49], v7, s[10:11] nt
	global_load_dwordx4 v[74:77], v9, s[4:5] offset:0 nt
	global_load_dwordx4 v[78:81], v9, s[4:5] offset:32 nt
	global_load_dwordx4 v[82:85], v9, s[4:5] offset:64 nt
	global_load_dwordx4 v[86:89], v9, s[4:5] offset:96 nt
	s_movk_i32 s3, 0x90
	v_lshlrev_b32_e32 v11, 3, v2
	v_mul_u32_u24_e32 v16, 0x1c8, v11
	v_mad_u32_u24 v12, v3, s3, v10
	v_lshl_add_u32 v13, v3, 1, v16
	v_mad_u32_u24 v112, v108, s3, v111
	s_waitcnt vmcnt(11)
	ds_write_b128 v12, v[18:21] offset:0
	s_waitcnt vmcnt(10)
	ds_write_b16 v13, v22 offset:32256
	ds_write_b16_d16_hi v13, v22 offset:32712
	ds_write_b16 v13, v23 offset:33168
	ds_write_b16_d16_hi v13, v23 offset:33624
	ds_write_b16 v13, v24 offset:34080
	ds_write_b16_d16_hi v13, v24 offset:34536
	ds_write_b16 v13, v25 offset:34992
	ds_write_b16_d16_hi v13, v25 offset:35448
	s_waitcnt vmcnt(9)
	ds_write_b128 v12, v[26:29] offset:8064
	s_waitcnt vmcnt(8)
	ds_write_b16 v13, v30 offset:32368
	ds_write_b16_d16_hi v13, v30 offset:32824
	ds_write_b16 v13, v31 offset:33280
	ds_write_b16_d16_hi v13, v31 offset:33736
	ds_write_b16 v13, v32 offset:34192
	ds_write_b16_d16_hi v13, v32 offset:34648
	ds_write_b16 v13, v33 offset:35104
	ds_write_b16_d16_hi v13, v33 offset:35560
	s_waitcnt vmcnt(7)
	ds_write_b128 v12, v[34:37] offset:16128
	s_waitcnt vmcnt(6)
	ds_write_b16 v13, v38 offset:32480
	ds_write_b16_d16_hi v13, v38 offset:32936
	ds_write_b16 v13, v39 offset:33392
	ds_write_b16_d16_hi v13, v39 offset:33848
	ds_write_b16 v13, v40 offset:34304
	ds_write_b16_d16_hi v13, v40 offset:34760
	ds_write_b16 v13, v41 offset:35216
	ds_write_b16_d16_hi v13, v41 offset:35672
	s_waitcnt vmcnt(5)
	v_cndmask_b32_e32 v42, 0, v42, vcc
	v_cndmask_b32_e32 v43, 0, v43, vcc
	v_cndmask_b32_e32 v44, 0, v44, vcc
	v_cndmask_b32_e32 v45, 0, v45, vcc
	ds_write_b128 v12, v[42:45] offset:24192
	s_waitcnt vmcnt(4)
	v_cndmask_b32_e32 v46, 0, v46, vcc
	v_cndmask_b32_e32 v47, 0, v47, vcc
	v_cndmask_b32_e32 v48, 0, v48, vcc
	v_cndmask_b32_e32 v49, 0, v49, vcc
	ds_write_b16 v13, v46 offset:32592
	ds_write_b16_d16_hi v13, v46 offset:33048
	ds_write_b16 v13, v47 offset:33504
	ds_write_b16_d16_hi v13, v47 offset:33960
	ds_write_b16 v13, v48 offset:34416
	ds_write_b16_d16_hi v13, v48 offset:34872
	ds_write_b16 v13, v49 offset:35328
	ds_write_b16_d16_hi v13, v49 offset:35784
	s_load_dwordx2 s[8:9], s[0:1], 0x20
	s_load_dwordx2 s[10:11], s[0:1], 0x18
	s_mov_b32 s16, 0x3e38aa3b
	s_mov_b32 s17, 0xf149f2ca
	v_cmp_eq_u32_e64 s[14:15], 0, v1
	v_mul_u32_u24_e32 v113, 0x1c8, v108
	v_lshl_add_u32 v113, v1, 3, v113
	v_add_u32_e32 v113, 0x7e00, v113
	v_add_u32_e32 v114, 0x3900, v113
	v_mov_b32_e32 v106, s17
	s_waitcnt vmcnt(0) lgkmcnt(0)
	s_barrier
	ds_read_b128 v[66:69], v112 offset:0
	ds_read_b128 v[70:73], v112 offset:32
	s_waitcnt lgkmcnt(1)
	v_mfma_f32_32x32x16_f16 v[2:17], v[66:69], v[74:77], 0
	ds_read_b128 v[66:69], v112 offset:64
	s_waitcnt lgkmcnt(1)
	v_mfma_f32_32x32x16_f16 v[2:17], v[70:73], v[78:81], v[2:17]
	ds_read_b128 v[70:73], v112 offset:96
	s_waitcnt lgkmcnt(1)
	v_mfma_f32_32x32x16_f16 v[2:17], v[66:69], v[82:85], v[2:17]
	s_waitcnt lgkmcnt(0)
	v_mfma_f32_32x32x16_f16 v[2:17], v[70:73], v[86:89], v[2:17]
	ds_read_b128 v[66:69], v112 offset:4608
	ds_read_b128 v[70:73], v112 offset:4640
	s_waitcnt lgkmcnt(1)
	v_mfma_f32_32x32x16_f16 v[18:33], v[66:69], v[74:77], 0
	ds_read_b128 v[66:69], v112 offset:4672
	s_waitcnt lgkmcnt(1)
	v_mfma_f32_32x32x16_f16 v[18:33], v[70:73], v[78:81], v[18:33]
	ds_read_b128 v[70:73], v112 offset:4704
	s_waitcnt lgkmcnt(1)
	v_mfma_f32_32x32x16_f16 v[18:33], v[66:69], v[82:85], v[18:33]
	s_waitcnt lgkmcnt(0)
	v_mfma_f32_32x32x16_f16 v[18:33], v[70:73], v[86:89], v[18:33]
	v_max3_f32 v106, v106, v2, v3
	v_max3_f32 v106, v106, v4, v5
	v_max3_f32 v106, v106, v6, v7
	v_max3_f32 v106, v106, v8, v9
	v_max3_f32 v106, v106, v10, v11
	v_max3_f32 v106, v106, v12, v13
	v_max3_f32 v106, v106, v14, v15
	v_max3_f32 v106, v106, v16, v17
	ds_read_b128 v[66:69], v112 offset:9216
	ds_read_b128 v[70:73], v112 offset:9248
	s_waitcnt lgkmcnt(1)
	v_mfma_f32_32x32x16_f16 v[2:17], v[66:69], v[74:77], 0
	ds_read_b128 v[66:69], v112 offset:9280
	s_waitcnt lgkmcnt(1)
	v_mfma_f32_32x32x16_f16 v[2:17], v[70:73], v[78:81], v[2:17]
	ds_read_b128 v[70:73], v112 offset:9312
	s_waitcnt lgkmcnt(1)
	v_mfma_f32_32x32x16_f16 v[2:17], v[66:69], v[82:85], v[2:17]
	s_waitcnt lgkmcnt(0)
	v_mfma_f32_32x32x16_f16 v[2:17], v[70:73], v[86:89], v[2:17]
	v_max3_f32 v106, v106, v18, v19
	v_max3_f32 v106, v106, v20, v21
	v_max3_f32 v106, v106, v22, v23
	v_max3_f32 v106, v106, v24, v25
	v_max3_f32 v106, v106, v26, v27
	v_max3_f32 v106, v106, v28, v29
	v_max3_f32 v106, v106, v30, v31
	v_max3_f32 v106, v106, v32, v33
	ds_read_b128 v[66:69], v112 offset:13824
	ds_read_b128 v[70:73], v112 offset:13856
	s_waitcnt lgkmcnt(1)
	v_mfma_f32_32x32x16_f16 v[18:33], v[66:69], v[74:77], 0
	ds_read_b128 v[66:69], v112 offset:13888
	s_waitcnt lgkmcnt(1)
	v_mfma_f32_32x32x16_f16 v[18:33], v[70:73], v[78:81], v[18:33]
	ds_read_b128 v[70:73], v112 offset:13920
	s_waitcnt lgkmcnt(1)
	v_mfma_f32_32x32x16_f16 v[18:33], v[66:69], v[82:85], v[18:33]
	s_waitcnt lgkmcnt(0)
	v_mfma_f32_32x32x16_f16 v[18:33], v[70:73], v[86:89], v[18:33]
	v_max3_f32 v106, v106, v2, v3
	v_max3_f32 v106, v106, v4, v5
	v_max3_f32 v106, v106, v6, v7
	v_max3_f32 v106, v106, v8, v9
	v_max3_f32 v106, v106, v10, v11
	v_max3_f32 v106, v106, v12, v13
	v_max3_f32 v106, v106, v14, v15
	v_max3_f32 v106, v106, v16, v17
	ds_read_b128 v[66:69], v112 offset:18432
	ds_read_b128 v[70:73], v112 offset:18464
	s_waitcnt lgkmcnt(1)
	v_mfma_f32_32x32x16_f16 v[2:17], v[66:69], v[74:77], 0
	ds_read_b128 v[66:69], v112 offset:18496
	s_waitcnt lgkmcnt(1)
	v_mfma_f32_32x32x16_f16 v[2:17], v[70:73], v[78:81], v[2:17]
	ds_read_b128 v[70:73], v112 offset:18528
	s_waitcnt lgkmcnt(1)
	v_mfma_f32_32x32x16_f16 v[2:17], v[66:69], v[82:85], v[2:17]
	s_waitcnt lgkmcnt(0)
	v_mfma_f32_32x32x16_f16 v[2:17], v[70:73], v[86:89], v[2:17]
	v_max3_f32 v106, v106, v18, v19
	v_max3_f32 v106, v106, v20, v21
	v_max3_f32 v106, v106, v22, v23
	v_max3_f32 v106, v106, v24, v25
	v_max3_f32 v106, v106, v26, v27
	v_max3_f32 v106, v106, v28, v29
	v_max3_f32 v106, v106, v30, v31
	v_max3_f32 v106, v106, v32, v33
	ds_read_b128 v[66:69], v112 offset:23040
	ds_read_b128 v[70:73], v112 offset:23072
	s_waitcnt lgkmcnt(1)
	v_mfma_f32_32x32x16_f16 v[18:33], v[66:69], v[74:77], 0
	ds_read_b128 v[66:69], v112 offset:23104
	s_waitcnt lgkmcnt(1)
	v_mfma_f32_32x32x16_f16 v[18:33], v[70:73], v[78:81], v[18:33]
	ds_read_b128 v[70:73], v112 offset:23136
	s_waitcnt lgkmcnt(1)
	v_mfma_f32_32x32x16_f16 v[18:33], v[66:69], v[82:85], v[18:33]
	s_waitcnt lgkmcnt(0)
	v_mfma_f32_32x32x16_f16 v[18:33], v[70:73], v[86:89], v[18:33]
	v_max3_f32 v106, v106, v2, v3
	v_max3_f32 v106, v106, v4, v5
	v_max3_f32 v106, v106, v6, v7
	v_max3_f32 v106, v106, v8, v9
	v_max3_f32 v106, v106, v10, v11
	v_max3_f32 v106, v106, v12, v13
	v_max3_f32 v106, v106, v14, v15
	v_max3_f32 v106, v106, v16, v17
	ds_read_b128 v[66:69], v112 offset:27648
	ds_read_b128 v[70:73], v112 offset:27680
	s_waitcnt lgkmcnt(1)
	v_mfma_f32_32x32x16_f16 v[2:17], v[66:69], v[74:77], 0
	ds_read_b128 v[66:69], v112 offset:27712
	s_waitcnt lgkmcnt(1)
	v_mfma_f32_32x32x16_f16 v[2:17], v[70:73], v[78:81], v[2:17]
	ds_read_b128 v[70:73], v112 offset:27744
	s_waitcnt lgkmcnt(1)
	v_mfma_f32_32x32x16_f16 v[2:17], v[66:69], v[82:85], v[2:17]
	s_waitcnt lgkmcnt(0)
	v_mfma_f32_32x32x16_f16 v[2:17], v[70:73], v[86:89], v[2:17]
	v_max3_f32 v106, v106, v18, v19
	v_max3_f32 v106, v106, v20, v21
	v_max3_f32 v106, v106, v22, v23
	v_max3_f32 v106, v106, v24, v25
	v_max3_f32 v106, v106, v26, v27
	v_max3_f32 v106, v106, v28, v29
	v_max3_f32 v106, v106, v30, v31
	v_max3_f32 v106, v106, v32, v33
	s_nop 15
	s_nop 1
	v_mov_b32_e32 v6, s17
	v_mov_b32_e32 v7, s17
	v_mov_b32_e32 v8, s17
	v_mov_b32_e32 v9, s17
	v_mov_b32_e32 v10, s17
	v_mov_b32_e32 v11, s17
	v_mov_b32_e32 v12, s17
	v_mov_b32_e32 v13, s17
	v_mov_b32_e32 v14, s17
	v_mov_b32_e32 v15, s17
	v_mov_b32_e32 v16, s17
	v_mov_b32_e32 v17, s17
	v_mov_b32_e32 v120, s17
	v_cndmask_b32_e64 v3, v120, v3, s[14:15]
	v_cndmask_b32_e64 v4, v120, v4, s[14:15]
	v_cndmask_b32_e64 v5, v120, v5, s[14:15]
	v_max3_f32 v106, v106, v2, v3
	v_max3_f32 v106, v106, v4, v5
	v_max3_f32 v106, v106, v6, v7
	v_max3_f32 v106, v106, v8, v9
	v_max3_f32 v106, v106, v10, v11
	v_max3_f32 v106, v106, v12, v13
	v_max3_f32 v106, v106, v14, v15
	v_max3_f32 v106, v106, v16, v17
	v_mov_b32_e32 v120, v106
	v_mov_b32_e32 v121, v106
	s_nop 1
	v_permlane32_swap_b32_e32 v120, v121
	s_nop 1
	v_max3_f32 v106, v106, v120, v121
	v_mul_f32_e32 v106, s16, v106
	v_mov_b32_e32 v107, 0
	v_mov_b32_e32 v18, 0
	v_mov_b32_e32 v19, 0
	v_mov_b32_e32 v20, 0
	v_mov_b32_e32 v21, 0
	v_mov_b32_e32 v22, 0
	v_mov_b32_e32 v23, 0
	v_mov_b32_e32 v24, 0
	v_mov_b32_e32 v25, 0
	v_mov_b32_e32 v26, 0
	v_mov_b32_e32 v27, 0
	v_mov_b32_e32 v28, 0
	v_mov_b32_e32 v29, 0
	v_mov_b32_e32 v30, 0
	v_mov_b32_e32 v31, 0
	v_mov_b32_e32 v32, 0
	v_mov_b32_e32 v33, 0
	v_mov_b32_e32 v34, 0
	v_mov_b32_e32 v35, 0
	v_mov_b32_e32 v36, 0
	v_mov_b32_e32 v37, 0
	v_mov_b32_e32 v38, 0
	v_mov_b32_e32 v39, 0
	v_mov_b32_e32 v40, 0
	v_mov_b32_e32 v41, 0
	v_mov_b32_e32 v42, 0
	v_mov_b32_e32 v43, 0
	v_mov_b32_e32 v44, 0
	v_mov_b32_e32 v45, 0
	v_mov_b32_e32 v46, 0
	v_mov_b32_e32 v47, 0
	v_mov_b32_e32 v48, 0
	v_mov_b32_e32 v49, 0
	ds_read_b128 v[66:69], v112 offset:0
	ds_read_b128 v[70:73], v112 offset:32
	s_waitcnt lgkmcnt(1)
	v_mfma_f32_32x32x16_f16 v[2:17], v[66:69], v[74:77], 0
	ds_read_b128 v[66:69], v112 offset:64
	s_waitcnt lgkmcnt(1)
	v_mfma_f32_32x32x16_f16 v[2:17], v[70:73], v[78:81], v[2:17]
	ds_read_b128 v[70:73], v112 offset:96
	s_waitcnt lgkmcnt(1)
	v_mfma_f32_32x32x16_f16 v[2:17], v[66:69], v[82:85], v[2:17]
	s_waitcnt lgkmcnt(0)
	v_mfma_f32_32x32x16_f16 v[2:17], v[70:73], v[86:89], v[2:17]
	ds_read_b128 v[66:69], v112 offset:4608
	ds_read_b128 v[70:73], v112 offset:4640
	s_waitcnt lgkmcnt(1)
	v_mfma_f32_32x32x16_f16 v[90:105], v[66:69], v[74:77], 0
	ds_read_b128 v[66:69], v112 offset:4672
	s_waitcnt lgkmcnt(1)
	v_mfma_f32_32x32x16_f16 v[90:105], v[70:73], v[78:81], v[90:105]
	ds_read_b128 v[70:73], v112 offset:4704
	s_waitcnt lgkmcnt(1)
	v_mfma_f32_32x32x16_f16 v[90:105], v[66:69], v[82:85], v[90:105]
	s_waitcnt lgkmcnt(0)
	v_mfma_f32_32x32x16_f16 v[90:105], v[70:73], v[86:89], v[90:105]
	v_fma_f32 v120, v2, s16, -v106
	v_exp_f32_e32 v2, v120
	v_fma_f32 v121, v3, s16, -v106
	v_exp_f32_e32 v3, v121
	v_fma_f32 v122, v4, s16, -v106
	v_exp_f32_e32 v4, v122
	v_fma_f32 v123, v5, s16, -v106
	v_exp_f32_e32 v5, v123
	v_fma_f32 v120, v6, s16, -v106
	v_exp_f32_e32 v6, v120
	v_fma_f32 v121, v7, s16, -v106
	v_exp_f32_e32 v7, v121
	v_fma_f32 v122, v8, s16, -v106
	v_exp_f32_e32 v8, v122
	v_fma_f32 v123, v9, s16, -v106
	v_exp_f32_e32 v9, v123
	v_fma_f32 v120, v10, s16, -v106
	v_exp_f32_e32 v10, v120
	v_fma_f32 v121, v11, s16, -v106
	v_exp_f32_e32 v11, v121
	v_fma_f32 v122, v12, s16, -v106
	v_exp_f32_e32 v12, v122
	v_fma_f32 v123, v13, s16, -v106
	v_exp_f32_e32 v13, v123
	v_fma_f32 v120, v14, s16, -v106
	v_exp_f32_e32 v14, v120
	v_fma_f32 v121, v15, s16, -v106
	v_exp_f32_e32 v15, v121
	v_fma_f32 v122, v16, s16, -v106
	v_exp_f32_e32 v16, v122
	v_fma_f32 v123, v17, s16, -v106
	v_exp_f32_e32 v17, v123
	v_add_f32_e32 v107, v107, v2
	v_add_f32_e32 v107, v107, v3
	v_add_f32_e32 v107, v107, v4
	v_add_f32_e32 v107, v107, v5
	v_add_f32_e32 v107, v107, v6
	v_add_f32_e32 v107, v107, v7
	v_add_f32_e32 v107, v107, v8
	v_add_f32_e32 v107, v107, v9
	v_add_f32_e32 v107, v107, v10
	v_add_f32_e32 v107, v107, v11
	v_add_f32_e32 v107, v107, v12
	v_add_f32_e32 v107, v107, v13
	v_add_f32_e32 v107, v107, v14
	v_add_f32_e32 v107, v107, v15
	v_add_f32_e32 v107, v107, v16
	v_add_f32_e32 v107, v107, v17
	ds_read2_b64 v[58:61], v113 offset0:0 offset1:2
	ds_read2_b64 v[62:65], v114 offset0:0 offset1:2
	v_cvt_pk_f16_f32 v50, v2, v3
	v_cvt_pk_f16_f32 v51, v4, v5
	v_cvt_pk_f16_f32 v52, v6, v7
	v_cvt_pk_f16_f32 v53, v8, v9
	v_cvt_pk_f16_f32 v54, v10, v11
	v_cvt_pk_f16_f32 v55, v12, v13
	v_cvt_pk_f16_f32 v56, v14, v15
	v_cvt_pk_f16_f32 v57, v16, v17
	s_nop 1
	s_waitcnt lgkmcnt(1)
	v_mfma_f32_32x32x16_f16 v[18:33], v[58:61], v[50:53], v[18:33]
	ds_read2_b64 v[58:61], v113 offset0:4 offset1:6
	s_waitcnt lgkmcnt(1)
	v_mfma_f32_32x32x16_f16 v[34:49], v[62:65], v[50:53], v[34:49]
	ds_read2_b64 v[62:65], v114 offset0:4 offset1:6
	s_waitcnt lgkmcnt(1)
	v_mfma_f32_32x32x16_f16 v[18:33], v[58:61], v[54:57], v[18:33]
	s_waitcnt lgkmcnt(0)
	v_mfma_f32_32x32x16_f16 v[34:49], v[62:65], v[54:57], v[34:49]
	ds_read_b128 v[66:69], v112 offset:9216
	ds_read_b128 v[70:73], v112 offset:9248
	s_waitcnt lgkmcnt(1)
	v_mfma_f32_32x32x16_f16 v[2:17], v[66:69], v[74:77], 0
	ds_read_b128 v[66:69], v112 offset:9280
	s_waitcnt lgkmcnt(1)
	v_mfma_f32_32x32x16_f16 v[2:17], v[70:73], v[78:81], v[2:17]
	ds_read_b128 v[70:73], v112 offset:9312
	s_waitcnt lgkmcnt(1)
	v_mfma_f32_32x32x16_f16 v[2:17], v[66:69], v[82:85], v[2:17]
	s_waitcnt lgkmcnt(0)
	v_mfma_f32_32x32x16_f16 v[2:17], v[70:73], v[86:89], v[2:17]
	v_fma_f32 v120, v90, s16, -v106
	v_exp_f32_e32 v90, v120
	v_fma_f32 v121, v91, s16, -v106
	v_exp_f32_e32 v91, v121
	v_fma_f32 v122, v92, s16, -v106
	v_exp_f32_e32 v92, v122
	v_fma_f32 v123, v93, s16, -v106
	v_exp_f32_e32 v93, v123
	v_fma_f32 v120, v94, s16, -v106
	v_exp_f32_e32 v94, v120
	v_fma_f32 v121, v95, s16, -v106
	v_exp_f32_e32 v95, v121
	v_fma_f32 v122, v96, s16, -v106
	v_exp_f32_e32 v96, v122
	v_fma_f32 v123, v97, s16, -v106
	v_exp_f32_e32 v97, v123
	v_fma_f32 v120, v98, s16, -v106
	v_exp_f32_e32 v98, v120
	v_fma_f32 v121, v99, s16, -v106
	v_exp_f32_e32 v99, v121
	v_fma_f32 v122, v100, s16, -v106
	v_exp_f32_e32 v100, v122
	v_fma_f32 v123, v101, s16, -v106
	v_exp_f32_e32 v101, v123
	v_fma_f32 v120, v102, s16, -v106
	v_exp_f32_e32 v102, v120
	v_fma_f32 v121, v103, s16, -v106
	v_exp_f32_e32 v103, v121
	v_fma_f32 v122, v104, s16, -v106
	v_exp_f32_e32 v104, v122
	v_fma_f32 v123, v105, s16, -v106
	v_exp_f32_e32 v105, v123
	v_add_f32_e32 v107, v107, v90
	v_add_f32_e32 v107, v107, v91
	v_add_f32_e32 v107, v107, v92
	v_add_f32_e32 v107, v107, v93
	v_add_f32_e32 v107, v107, v94
	v_add_f32_e32 v107, v107, v95
	v_add_f32_e32 v107, v107, v96
	v_add_f32_e32 v107, v107, v97
	v_add_f32_e32 v107, v107, v98
	v_add_f32_e32 v107, v107, v99
	v_add_f32_e32 v107, v107, v100
	v_add_f32_e32 v107, v107, v101
	v_add_f32_e32 v107, v107, v102
	v_add_f32_e32 v107, v107, v103
	v_add_f32_e32 v107, v107, v104
	v_add_f32_e32 v107, v107, v105
	ds_read2_b64 v[58:61], v113 offset0:8 offset1:10
	ds_read2_b64 v[62:65], v114 offset0:8 offset1:10
	v_cvt_pk_f16_f32 v50, v90, v91
	v_cvt_pk_f16_f32 v51, v92, v93
	v_cvt_pk_f16_f32 v52, v94, v95
	v_cvt_pk_f16_f32 v53, v96, v97
	v_cvt_pk_f16_f32 v54, v98, v99
	v_cvt_pk_f16_f32 v55, v100, v101
	v_cvt_pk_f16_f32 v56, v102, v103
	v_cvt_pk_f16_f32 v57, v104, v105
	s_nop 1
	s_waitcnt lgkmcnt(1)
	v_mfma_f32_32x32x16_f16 v[18:33], v[58:61], v[50:53], v[18:33]
	ds_read2_b64 v[58:61], v113 offset0:12 offset1:14
	s_waitcnt lgkmcnt(1)
	v_mfma_f32_32x32x16_f16 v[34:49], v[62:65], v[50:53], v[34:49]
	ds_read2_b64 v[62:65], v114 offset0:12 offset1:14
	s_waitcnt lgkmcnt(1)
	v_mfma_f32_32x32x16_f16 v[18:33], v[58:61], v[54:57], v[18:33]
	s_waitcnt lgkmcnt(0)
	v_mfma_f32_32x32x16_f16 v[34:49], v[62:65], v[54:57], v[34:49]
	ds_read_b128 v[66:69], v112 offset:13824
	ds_read_b128 v[70:73], v112 offset:13856
	s_waitcnt lgkmcnt(1)
	v_mfma_f32_32x32x16_f16 v[90:105], v[66:69], v[74:77], 0
	ds_read_b128 v[66:69], v112 offset:13888
	s_waitcnt lgkmcnt(1)
	v_mfma_f32_32x32x16_f16 v[90:105], v[70:73], v[78:81], v[90:105]
	ds_read_b128 v[70:73], v112 offset:13920
	s_waitcnt lgkmcnt(1)
	v_mfma_f32_32x32x16_f16 v[90:105], v[66:69], v[82:85], v[90:105]
	s_waitcnt lgkmcnt(0)
	v_mfma_f32_32x32x16_f16 v[90:105], v[70:73], v[86:89], v[90:105]
	v_fma_f32 v120, v2, s16, -v106
	v_exp_f32_e32 v2, v120
	v_fma_f32 v121, v3, s16, -v106
	v_exp_f32_e32 v3, v121
	v_fma_f32 v122, v4, s16, -v106
	v_exp_f32_e32 v4, v122
	v_fma_f32 v123, v5, s16, -v106
	v_exp_f32_e32 v5, v123
	v_fma_f32 v120, v6, s16, -v106
	v_exp_f32_e32 v6, v120
	v_fma_f32 v121, v7, s16, -v106
	v_exp_f32_e32 v7, v121
	v_fma_f32 v122, v8, s16, -v106
	v_exp_f32_e32 v8, v122
	v_fma_f32 v123, v9, s16, -v106
	v_exp_f32_e32 v9, v123
	v_fma_f32 v120, v10, s16, -v106
	v_exp_f32_e32 v10, v120
	v_fma_f32 v121, v11, s16, -v106
	v_exp_f32_e32 v11, v121
	v_fma_f32 v122, v12, s16, -v106
	v_exp_f32_e32 v12, v122
	v_fma_f32 v123, v13, s16, -v106
	v_exp_f32_e32 v13, v123
	v_fma_f32 v120, v14, s16, -v106
	v_exp_f32_e32 v14, v120
	v_fma_f32 v121, v15, s16, -v106
	v_exp_f32_e32 v15, v121
	v_fma_f32 v122, v16, s16, -v106
	v_exp_f32_e32 v16, v122
	v_fma_f32 v123, v17, s16, -v106
	v_exp_f32_e32 v17, v123
	v_add_f32_e32 v107, v107, v2
	v_add_f32_e32 v107, v107, v3
	v_add_f32_e32 v107, v107, v4
	v_add_f32_e32 v107, v107, v5
	v_add_f32_e32 v107, v107, v6
	v_add_f32_e32 v107, v107, v7
	v_add_f32_e32 v107, v107, v8
	v_add_f32_e32 v107, v107, v9
	v_add_f32_e32 v107, v107, v10
	v_add_f32_e32 v107, v107, v11
	v_add_f32_e32 v107, v107, v12
	v_add_f32_e32 v107, v107, v13
	v_add_f32_e32 v107, v107, v14
	v_add_f32_e32 v107, v107, v15
	v_add_f32_e32 v107, v107, v16
	v_add_f32_e32 v107, v107, v17
	ds_read2_b64 v[58:61], v113 offset0:16 offset1:18
	ds_read2_b64 v[62:65], v114 offset0:16 offset1:18
	v_cvt_pk_f16_f32 v50, v2, v3
	v_cvt_pk_f16_f32 v51, v4, v5
	v_cvt_pk_f16_f32 v52, v6, v7
	v_cvt_pk_f16_f32 v53, v8, v9
	v_cvt_pk_f16_f32 v54, v10, v11
	v_cvt_pk_f16_f32 v55, v12, v13
	v_cvt_pk_f16_f32 v56, v14, v15
	v_cvt_pk_f16_f32 v57, v16, v17
	s_nop 1
	s_waitcnt lgkmcnt(1)
	v_mfma_f32_32x32x16_f16 v[18:33], v[58:61], v[50:53], v[18:33]
	ds_read2_b64 v[58:61], v113 offset0:20 offset1:22
	s_waitcnt lgkmcnt(1)
	v_mfma_f32_32x32x16_f16 v[34:49], v[62:65], v[50:53], v[34:49]
	ds_read2_b64 v[62:65], v114 offset0:20 offset1:22
	s_waitcnt lgkmcnt(1)
	v_mfma_f32_32x32x16_f16 v[18:33], v[58:61], v[54:57], v[18:33]
	s_waitcnt lgkmcnt(0)
	v_mfma_f32_32x32x16_f16 v[34:49], v[62:65], v[54:57], v[34:49]
	ds_read_b128 v[66:69], v112 offset:18432
	ds_read_b128 v[70:73], v112 offset:18464
	s_waitcnt lgkmcnt(1)
	v_mfma_f32_32x32x16_f16 v[2:17], v[66:69], v[74:77], 0
	ds_read_b128 v[66:69], v112 offset:18496
	s_waitcnt lgkmcnt(1)
	v_mfma_f32_32x32x16_f16 v[2:17], v[70:73], v[78:81], v[2:17]
	ds_read_b128 v[70:73], v112 offset:18528
	s_waitcnt lgkmcnt(1)
	v_mfma_f32_32x32x16_f16 v[2:17], v[66:69], v[82:85], v[2:17]
	s_waitcnt lgkmcnt(0)
	v_mfma_f32_32x32x16_f16 v[2:17], v[70:73], v[86:89], v[2:17]
	v_fma_f32 v120, v90, s16, -v106
	v_exp_f32_e32 v90, v120
	v_fma_f32 v121, v91, s16, -v106
	v_exp_f32_e32 v91, v121
	v_fma_f32 v122, v92, s16, -v106
	v_exp_f32_e32 v92, v122
	v_fma_f32 v123, v93, s16, -v106
	v_exp_f32_e32 v93, v123
	v_fma_f32 v120, v94, s16, -v106
	v_exp_f32_e32 v94, v120
	v_fma_f32 v121, v95, s16, -v106
	v_exp_f32_e32 v95, v121
	v_fma_f32 v122, v96, s16, -v106
	v_exp_f32_e32 v96, v122
	v_fma_f32 v123, v97, s16, -v106
	v_exp_f32_e32 v97, v123
	v_fma_f32 v120, v98, s16, -v106
	v_exp_f32_e32 v98, v120
	v_fma_f32 v121, v99, s16, -v106
	v_exp_f32_e32 v99, v121
	v_fma_f32 v122, v100, s16, -v106
	v_exp_f32_e32 v100, v122
	v_fma_f32 v123, v101, s16, -v106
	v_exp_f32_e32 v101, v123
	v_fma_f32 v120, v102, s16, -v106
	v_exp_f32_e32 v102, v120
	v_fma_f32 v121, v103, s16, -v106
	v_exp_f32_e32 v103, v121
	v_fma_f32 v122, v104, s16, -v106
	v_exp_f32_e32 v104, v122
	v_fma_f32 v123, v105, s16, -v106
	v_exp_f32_e32 v105, v123
	v_add_f32_e32 v107, v107, v90
	v_add_f32_e32 v107, v107, v91
	v_add_f32_e32 v107, v107, v92
	v_add_f32_e32 v107, v107, v93
	v_add_f32_e32 v107, v107, v94
	v_add_f32_e32 v107, v107, v95
	v_add_f32_e32 v107, v107, v96
	v_add_f32_e32 v107, v107, v97
	v_add_f32_e32 v107, v107, v98
	v_add_f32_e32 v107, v107, v99
	v_add_f32_e32 v107, v107, v100
	v_add_f32_e32 v107, v107, v101
	v_add_f32_e32 v107, v107, v102
	v_add_f32_e32 v107, v107, v103
	v_add_f32_e32 v107, v107, v104
	v_add_f32_e32 v107, v107, v105
	ds_read2_b64 v[58:61], v113 offset0:24 offset1:26
	ds_read2_b64 v[62:65], v114 offset0:24 offset1:26
	v_cvt_pk_f16_f32 v50, v90, v91
	v_cvt_pk_f16_f32 v51, v92, v93
	v_cvt_pk_f16_f32 v52, v94, v95
	v_cvt_pk_f16_f32 v53, v96, v97
	v_cvt_pk_f16_f32 v54, v98, v99
	v_cvt_pk_f16_f32 v55, v100, v101
	v_cvt_pk_f16_f32 v56, v102, v103
	v_cvt_pk_f16_f32 v57, v104, v105
	s_nop 1
	s_waitcnt lgkmcnt(1)
	v_mfma_f32_32x32x16_f16 v[18:33], v[58:61], v[50:53], v[18:33]
	ds_read2_b64 v[58:61], v113 offset0:28 offset1:30
	s_waitcnt lgkmcnt(1)
	v_mfma_f32_32x32x16_f16 v[34:49], v[62:65], v[50:53], v[34:49]
	ds_read2_b64 v[62:65], v114 offset0:28 offset1:30
	s_waitcnt lgkmcnt(1)
	v_mfma_f32_32x32x16_f16 v[18:33], v[58:61], v[54:57], v[18:33]
	s_waitcnt lgkmcnt(0)
	v_mfma_f32_32x32x16_f16 v[34:49], v[62:65], v[54:57], v[34:49]
	ds_read_b128 v[66:69], v112 offset:23040
	ds_read_b128 v[70:73], v112 offset:23072
	s_waitcnt lgkmcnt(1)
	v_mfma_f32_32x32x16_f16 v[90:105], v[66:69], v[74:77], 0
	ds_read_b128 v[66:69], v112 offset:23104
	s_waitcnt lgkmcnt(1)
	v_mfma_f32_32x32x16_f16 v[90:105], v[70:73], v[78:81], v[90:105]
	ds_read_b128 v[70:73], v112 offset:23136
	s_waitcnt lgkmcnt(1)
	v_mfma_f32_32x32x16_f16 v[90:105], v[66:69], v[82:85], v[90:105]
	s_waitcnt lgkmcnt(0)
	v_mfma_f32_32x32x16_f16 v[90:105], v[70:73], v[86:89], v[90:105]
	v_fma_f32 v120, v2, s16, -v106
	v_exp_f32_e32 v2, v120
	v_fma_f32 v121, v3, s16, -v106
	v_exp_f32_e32 v3, v121
	v_fma_f32 v122, v4, s16, -v106
	v_exp_f32_e32 v4, v122
	v_fma_f32 v123, v5, s16, -v106
	v_exp_f32_e32 v5, v123
	v_fma_f32 v120, v6, s16, -v106
	v_exp_f32_e32 v6, v120
	v_fma_f32 v121, v7, s16, -v106
	v_exp_f32_e32 v7, v121
	v_fma_f32 v122, v8, s16, -v106
	v_exp_f32_e32 v8, v122
	v_fma_f32 v123, v9, s16, -v106
	v_exp_f32_e32 v9, v123
	v_fma_f32 v120, v10, s16, -v106
	v_exp_f32_e32 v10, v120
	v_fma_f32 v121, v11, s16, -v106
	v_exp_f32_e32 v11, v121
	v_fma_f32 v122, v12, s16, -v106
	v_exp_f32_e32 v12, v122
	v_fma_f32 v123, v13, s16, -v106
	v_exp_f32_e32 v13, v123
	v_fma_f32 v120, v14, s16, -v106
	v_exp_f32_e32 v14, v120
	v_fma_f32 v121, v15, s16, -v106
	v_exp_f32_e32 v15, v121
	v_fma_f32 v122, v16, s16, -v106
	v_exp_f32_e32 v16, v122
	v_fma_f32 v123, v17, s16, -v106
	v_exp_f32_e32 v17, v123
	v_add_f32_e32 v107, v107, v2
	v_add_f32_e32 v107, v107, v3
	v_add_f32_e32 v107, v107, v4
	v_add_f32_e32 v107, v107, v5
	v_add_f32_e32 v107, v107, v6
	v_add_f32_e32 v107, v107, v7
	v_add_f32_e32 v107, v107, v8
	v_add_f32_e32 v107, v107, v9
	v_add_f32_e32 v107, v107, v10
	v_add_f32_e32 v107, v107, v11
	v_add_f32_e32 v107, v107, v12
	v_add_f32_e32 v107, v107, v13
	v_add_f32_e32 v107, v107, v14
	v_add_f32_e32 v107, v107, v15
	v_add_f32_e32 v107, v107, v16
	v_add_f32_e32 v107, v107, v17
	ds_read2_b64 v[58:61], v113 offset0:32 offset1:34
	ds_read2_b64 v[62:65], v114 offset0:32 offset1:34
	v_cvt_pk_f16_f32 v50, v2, v3
	v_cvt_pk_f16_f32 v51, v4, v5
	v_cvt_pk_f16_f32 v52, v6, v7
	v_cvt_pk_f16_f32 v53, v8, v9
	v_cvt_pk_f16_f32 v54, v10, v11
	v_cvt_pk_f16_f32 v55, v12, v13
	v_cvt_pk_f16_f32 v56, v14, v15
	v_cvt_pk_f16_f32 v57, v16, v17
	s_nop 1
	s_waitcnt lgkmcnt(1)
	v_mfma_f32_32x32x16_f16 v[18:33], v[58:61], v[50:53], v[18:33]
	ds_read2_b64 v[58:61], v113 offset0:36 offset1:38
	s_waitcnt lgkmcnt(1)
	v_mfma_f32_32x32x16_f16 v[34:49], v[62:65], v[50:53], v[34:49]
	ds_read2_b64 v[62:65], v114 offset0:36 offset1:38
	s_waitcnt lgkmcnt(1)
	v_mfma_f32_32x32x16_f16 v[18:33], v[58:61], v[54:57], v[18:33]
	s_waitcnt lgkmcnt(0)
	v_mfma_f32_32x32x16_f16 v[34:49], v[62:65], v[54:57], v[34:49]
	ds_read_b128 v[66:69], v112 offset:27648
	ds_read_b128 v[70:73], v112 offset:27680
	s_waitcnt lgkmcnt(1)
	v_mfma_f32_32x32x16_f16 v[2:17], v[66:69], v[74:77], 0
	ds_read_b128 v[66:69], v112 offset:27712
	s_waitcnt lgkmcnt(1)
	v_mfma_f32_32x32x16_f16 v[2:17], v[70:73], v[78:81], v[2:17]
	ds_read_b128 v[70:73], v112 offset:27744
	s_waitcnt lgkmcnt(1)
	v_mfma_f32_32x32x16_f16 v[2:17], v[66:69], v[82:85], v[2:17]
	s_waitcnt lgkmcnt(0)
	v_mfma_f32_32x32x16_f16 v[2:17], v[70:73], v[86:89], v[2:17]
	v_fma_f32 v120, v90, s16, -v106
	v_exp_f32_e32 v90, v120
	v_fma_f32 v121, v91, s16, -v106
	v_exp_f32_e32 v91, v121
	v_fma_f32 v122, v92, s16, -v106
	v_exp_f32_e32 v92, v122
	v_fma_f32 v123, v93, s16, -v106
	v_exp_f32_e32 v93, v123
	v_fma_f32 v120, v94, s16, -v106
	v_exp_f32_e32 v94, v120
	v_fma_f32 v121, v95, s16, -v106
	v_exp_f32_e32 v95, v121
	v_fma_f32 v122, v96, s16, -v106
	v_exp_f32_e32 v96, v122
	v_fma_f32 v123, v97, s16, -v106
	v_exp_f32_e32 v97, v123
	v_fma_f32 v120, v98, s16, -v106
	v_exp_f32_e32 v98, v120
	v_fma_f32 v121, v99, s16, -v106
	v_exp_f32_e32 v99, v121
	v_fma_f32 v122, v100, s16, -v106
	v_exp_f32_e32 v100, v122
	v_fma_f32 v123, v101, s16, -v106
	v_exp_f32_e32 v101, v123
	v_fma_f32 v120, v102, s16, -v106
	v_exp_f32_e32 v102, v120
	v_fma_f32 v121, v103, s16, -v106
	v_exp_f32_e32 v103, v121
	v_fma_f32 v122, v104, s16, -v106
	v_exp_f32_e32 v104, v122
	v_fma_f32 v123, v105, s16, -v106
	v_exp_f32_e32 v105, v123
	v_add_f32_e32 v107, v107, v90
	v_add_f32_e32 v107, v107, v91
	v_add_f32_e32 v107, v107, v92
	v_add_f32_e32 v107, v107, v93
	v_add_f32_e32 v107, v107, v94
	v_add_f32_e32 v107, v107, v95
	v_add_f32_e32 v107, v107, v96
	v_add_f32_e32 v107, v107, v97
	v_add_f32_e32 v107, v107, v98
	v_add_f32_e32 v107, v107, v99
	v_add_f32_e32 v107, v107, v100
	v_add_f32_e32 v107, v107, v101
	v_add_f32_e32 v107, v107, v102
	v_add_f32_e32 v107, v107, v103
	v_add_f32_e32 v107, v107, v104
	v_add_f32_e32 v107, v107, v105
	ds_read2_b64 v[58:61], v113 offset0:40 offset1:42
	ds_read2_b64 v[62:65], v114 offset0:40 offset1:42
	v_cvt_pk_f16_f32 v50, v90, v91
	v_cvt_pk_f16_f32 v51, v92, v93
	v_cvt_pk_f16_f32 v52, v94, v95
	v_cvt_pk_f16_f32 v53, v96, v97
	v_cvt_pk_f16_f32 v54, v98, v99
	v_cvt_pk_f16_f32 v55, v100, v101
	v_cvt_pk_f16_f32 v56, v102, v103
	v_cvt_pk_f16_f32 v57, v104, v105
	s_nop 1
	s_waitcnt lgkmcnt(1)
	v_mfma_f32_32x32x16_f16 v[18:33], v[58:61], v[50:53], v[18:33]
	ds_read2_b64 v[58:61], v113 offset0:44 offset1:46
	s_waitcnt lgkmcnt(1)
	v_mfma_f32_32x32x16_f16 v[34:49], v[62:65], v[50:53], v[34:49]
	ds_read2_b64 v[62:65], v114 offset0:44 offset1:46
	s_waitcnt lgkmcnt(1)
	v_mfma_f32_32x32x16_f16 v[18:33], v[58:61], v[54:57], v[18:33]
	s_waitcnt lgkmcnt(0)
	v_mfma_f32_32x32x16_f16 v[34:49], v[62:65], v[54:57], v[34:49]
	s_nop 15
	s_nop 1
	v_mov_b32_e32 v6, s17
	v_mov_b32_e32 v7, s17
	v_mov_b32_e32 v8, s17
	v_mov_b32_e32 v9, s17
	v_mov_b32_e32 v10, s17
	v_mov_b32_e32 v11, s17
	v_mov_b32_e32 v12, s17
	v_mov_b32_e32 v13, s17
	v_mov_b32_e32 v14, s17
	v_mov_b32_e32 v15, s17
	v_mov_b32_e32 v16, s17
	v_mov_b32_e32 v17, s17
	v_mov_b32_e32 v120, s17
	v_cndmask_b32_e64 v3, v120, v3, s[14:15]
	v_cndmask_b32_e64 v4, v120, v4, s[14:15]
	v_cndmask_b32_e64 v5, v120, v5, s[14:15]
	v_fma_f32 v120, v2, s16, -v106
	v_exp_f32_e32 v2, v120
	v_fma_f32 v121, v3, s16, -v106
	v_exp_f32_e32 v3, v121
	v_fma_f32 v122, v4, s16, -v106
	v_exp_f32_e32 v4, v122
	v_fma_f32 v123, v5, s16, -v106
	v_exp_f32_e32 v5, v123
	v_fma_f32 v120, v6, s16, -v106
	v_exp_f32_e32 v6, v120
	v_fma_f32 v121, v7, s16, -v106
	v_exp_f32_e32 v7, v121
	v_fma_f32 v122, v8, s16, -v106
	v_exp_f32_e32 v8, v122
	v_fma_f32 v123, v9, s16, -v106
	v_exp_f32_e32 v9, v123
	v_fma_f32 v120, v10, s16, -v106
	v_exp_f32_e32 v10, v120
	v_fma_f32 v121, v11, s16, -v106
	v_exp_f32_e32 v11, v121
	v_fma_f32 v122, v12, s16, -v106
	v_exp_f32_e32 v12, v122
	v_fma_f32 v123, v13, s16, -v106
	v_exp_f32_e32 v13, v123
	v_fma_f32 v120, v14, s16, -v106
	v_exp_f32_e32 v14, v120
	v_fma_f32 v121, v15, s16, -v106
	v_exp_f32_e32 v15, v121
	v_fma_f32 v122, v16, s16, -v106
	v_exp_f32_e32 v16, v122
	v_fma_f32 v123, v17, s16, -v106
	v_exp_f32_e32 v17, v123
	v_add_f32_e32 v107, v107, v2
	v_add_f32_e32 v107, v107, v3
	v_add_f32_e32 v107, v107, v4
	v_add_f32_e32 v107, v107, v5
	v_add_f32_e32 v107, v107, v6
	v_add_f32_e32 v107, v107, v7
	v_add_f32_e32 v107, v107, v8
	v_add_f32_e32 v107, v107, v9
	v_add_f32_e32 v107, v107, v10
	v_add_f32_e32 v107, v107, v11
	v_add_f32_e32 v107, v107, v12
	v_add_f32_e32 v107, v107, v13
	v_add_f32_e32 v107, v107, v14
	v_add_f32_e32 v107, v107, v15
	v_add_f32_e32 v107, v107, v16
	v_add_f32_e32 v107, v107, v17
	ds_read2_b64 v[58:61], v113 offset0:48 offset1:50
	ds_read2_b64 v[62:65], v114 offset0:48 offset1:50
	v_cvt_pk_f16_f32 v50, v2, v3
	v_cvt_pk_f16_f32 v51, v4, v5
	v_cvt_pk_f16_f32 v52, v6, v7
	v_cvt_pk_f16_f32 v53, v8, v9
	v_cvt_pk_f16_f32 v54, v10, v11
	v_cvt_pk_f16_f32 v55, v12, v13
	v_cvt_pk_f16_f32 v56, v14, v15
	v_cvt_pk_f16_f32 v57, v16, v17
	s_nop 1
	s_waitcnt lgkmcnt(1)
	v_mfma_f32_32x32x16_f16 v[18:33], v[58:61], v[50:53], v[18:33]
	ds_read2_b64 v[58:61], v113 offset0:52 offset1:54
	s_waitcnt lgkmcnt(1)
	v_mfma_f32_32x32x16_f16 v[34:49], v[62:65], v[50:53], v[34:49]
	ds_read2_b64 v[62:65], v114 offset0:52 offset1:54
	s_waitcnt lgkmcnt(1)
	v_mfma_f32_32x32x16_f16 v[18:33], v[58:61], v[54:57], v[18:33]
	s_waitcnt lgkmcnt(0)
	v_mfma_f32_32x32x16_f16 v[34:49], v[62:65], v[54:57], v[34:49]
	v_mov_b32_e32 v120, v107
	v_mov_b32_e32 v121, v107
	s_nop 1
	v_permlane32_swap_b32_e32 v120, v121
	s_nop 1
	v_add_f32_e32 v107, v120, v121
	v_log_f32_e32 v122, v107
	v_rcp_f32_e32 v123, v107
	s_nop 0
	v_add_f32_e32 v122, v122, v106
	v_fma_f32 v124, -v107, v123, 2.0
	v_mul_f32_e32 v123, v123, v124
	v_lshlrev_b32_e32 v125, 2, v109
	s_mov_b64 s[18:19], exec
	s_and_b64 exec, exec, s[14:15]
	ds_write_b32 v125, v122 offset:61440
	s_mov_b64 exec, s[18:19]
	s_mul_i32 s20, s2, 0x493
	s_lshr_b32 s20, s20, 16
	s_mul_i32 s21, s20, 56
	s_sub_u32 s21, s2, s21
	s_mul_i32 s22, s21, 0x2493
	s_lshr_b32 s22, s22, 16
	s_mul_i32 s23, s22, 7
	s_sub_u32 s23, s21, s23
	s_mul_i32 s24, s23, 0xc5
	s_lshl_b32 s24, s24, 13
	s_lshl_b32 s25, s22, 10
	s_add_u32 s24, s24, s25
	s_lshl_b32 s25, s20, 7
	s_add_u32 s24, s24, s25
	v_lshlrev_b32_e32 v125, 13, v110
	v_add3_u32 v125, v125, s24, v111
	s_nop 15
	s_waitcnt lgkmcnt(0)
	v_mul_f32_e32 v18, v18, v123
	v_mul_f32_e32 v19, v19, v123
	v_mul_f32_e32 v20, v20, v123
	v_mul_f32_e32 v21, v21, v123
	v_mul_f32_e32 v22, v22, v123
	v_mul_f32_e32 v23, v23, v123
	v_mul_f32_e32 v24, v24, v123
	v_mul_f32_e32 v25, v25, v123
	v_cvt_pk_f16_f32 v50, v18, v19
	v_cvt_pk_f16_f32 v51, v20, v21
	v_cvt_pk_f16_f32 v52, v22, v23
	v_cvt_pk_f16_f32 v53, v24, v25
	s_nop 1
	v_permlane32_swap_b32_e32 v50, v52
	v_permlane32_swap_b32_e32 v51, v53
	s_nop 1
	s_and_b64 exec, exec, s[12:13]
	global_store_dwordx4 v125, v[50:53], s[8:9] offset:0
	s_mov_b64 exec, s[18:19]
	s_nop 1
	v_mul_f32_e32 v26, v26, v123
	v_mul_f32_e32 v27, v27, v123
	v_mul_f32_e32 v28, v28, v123
	v_mul_f32_e32 v29, v29, v123
	v_mul_f32_e32 v30, v30, v123
	v_mul_f32_e32 v31, v31, v123
	v_mul_f32_e32 v32, v32, v123
	v_mul_f32_e32 v33, v33, v123
	v_cvt_pk_f16_f32 v54, v26, v27
	v_cvt_pk_f16_f32 v55, v28, v29
	v_cvt_pk_f16_f32 v56, v30, v31
	v_cvt_pk_f16_f32 v57, v32, v33
	s_nop 1
	v_permlane32_swap_b32_e32 v54, v56
	v_permlane32_swap_b32_e32 v55, v57
	s_nop 1
	s_and_b64 exec, exec, s[12:13]
	global_store_dwordx4 v125, v[54:57], s[8:9] offset:32
	s_mov_b64 exec, s[18:19]
	s_nop 1
	v_mul_f32_e32 v34, v34, v123
	v_mul_f32_e32 v35, v35, v123
	v_mul_f32_e32 v36, v36, v123
	v_mul_f32_e32 v37, v37, v123
	v_mul_f32_e32 v38, v38, v123
	v_mul_f32_e32 v39, v39, v123
	v_mul_f32_e32 v40, v40, v123
	v_mul_f32_e32 v41, v41, v123
	v_cvt_pk_f16_f32 v50, v34, v35
	v_cvt_pk_f16_f32 v51, v36, v37
	v_cvt_pk_f16_f32 v52, v38, v39
	v_cvt_pk_f16_f32 v53, v40, v41
	s_nop 1
	v_permlane32_swap_b32_e32 v50, v52
	v_permlane32_swap_b32_e32 v51, v53
	s_nop 1
	s_and_b64 exec, exec, s[12:13]
	global_store_dwordx4 v125, v[50:53], s[8:9] offset:64
	s_mov_b64 exec, s[18:19]
	s_nop 1
	v_mul_f32_e32 v42, v42, v123
	v_mul_f32_e32 v43, v43, v123
	v_mul_f32_e32 v44, v44, v123
	v_mul_f32_e32 v45, v45, v123
	v_mul_f32_e32 v46, v46, v123
	v_mul_f32_e32 v47, v47, v123
	v_mul_f32_e32 v48, v48, v123
	v_mul_f32_e32 v49, v49, v123
	v_cvt_pk_f16_f32 v54, v42, v43
	v_cvt_pk_f16_f32 v55, v44, v45
	v_cvt_pk_f16_f32 v56, v46, v47
	v_cvt_pk_f16_f32 v57, v48, v49
	s_nop 1
	v_permlane32_swap_b32_e32 v54, v56
	v_permlane32_swap_b32_e32 v55, v57
	s_nop 1
	s_and_b64 exec, exec, s[12:13]
	global_store_dwordx4 v125, v[54:57], s[8:9] offset:96
	s_mov_b64 exec, s[18:19]
	s_nop 1
	s_waitcnt lgkmcnt(0)
	s_barrier
	v_lshl_add_u32 v120, v115, 2, v111
	ds_read_b128 v[90:93], v120 offset:61440
	ds_read_b128 v[94:97], v120 offset:61472
	ds_read_b128 v[98:101], v120 offset:61504
	ds_read_b128 v[102:105], v120 offset:61536
	v_lshl_or_b32 v121, v1, 2, v115
	v_mul_u32_u24_e32 v121, 0xc5, v121
	v_add_lshl_u32 v116, v121, v108, 2
	v_add_u32_e32 v117, 0x18a0, v116
	v_add_u32_e32 v118, 0x3140, v116
	v_add_u32_e32 v119, 0x49e0, v116
	s_mul_hi_u32 s21, s2, 0x25e64
	s_mul_i32 s20, s2, 0x25e64
	s_add_u32 s10, s10, s20
	s_addc_u32 s11, s11, s21
	v_cmp_gt_u32_e64 s[22:23], 5, v108
	s_nop 0
	v_readfirstlane_b32 s26, v115
	s_cmp_eq_u32 s26, 0xc0
	s_cbranch_scc1 .Lsp_wave6
	ds_read_b128 v[66:69], v112 offset:0
	ds_read_b128 v[70:73], v112 offset:32
	s_waitcnt lgkmcnt(1)
	v_mfma_f32_32x32x16_f16 v[2:17], v[74:77], v[66:69], 0
	ds_read_b128 v[66:69], v112 offset:64
	s_waitcnt lgkmcnt(1)
	v_mfma_f32_32x32x16_f16 v[2:17], v[78:81], v[70:73], v[2:17]
	ds_read_b128 v[70:73], v112 offset:96
	s_waitcnt lgkmcnt(1)
	v_mfma_f32_32x32x16_f16 v[2:17], v[82:85], v[66:69], v[2:17]
	s_waitcnt lgkmcnt(0)
	v_mfma_f32_32x32x16_f16 v[2:17], v[86:89], v[70:73], v[2:17]
	s_waitcnt lgkmcnt(0)
	ds_read_b128 v[66:69], v112 offset:4608
	ds_read_b128 v[70:73], v112 offset:4640
	s_waitcnt lgkmcnt(1)
	v_mfma_f32_32x32x16_f16 v[18:33], v[74:77], v[66:69], 0
	ds_read_b128 v[66:69], v112 offset:4672
	s_waitcnt lgkmcnt(1)
	v_mfma_f32_32x32x16_f16 v[18:33], v[78:81], v[70:73], v[18:33]
	ds_read_b128 v[70:73], v112 offset:4704
	s_waitcnt lgkmcnt(1)
	v_mfma_f32_32x32x16_f16 v[18:33], v[82:85], v[66:69], v[18:33]
	s_waitcnt lgkmcnt(0)
	v_mfma_f32_32x32x16_f16 v[18:33], v[86:89], v[70:73], v[18:33]
	v_fma_f32 v120, v2, s16, -v90
	v_exp_f32_e32 v2, v120
	v_fma_f32 v121, v3, s16, -v91
	v_exp_f32_e32 v3, v121
	v_fma_f32 v122, v4, s16, -v92
	v_exp_f32_e32 v4, v122
	v_fma_f32 v123, v5, s16, -v93
	v_exp_f32_e32 v5, v123
	v_fma_f32 v120, v6, s16, -v94
	v_exp_f32_e32 v6, v120
	v_fma_f32 v121, v7, s16, -v95
	v_exp_f32_e32 v7, v121
	v_fma_f32 v122, v8, s16, -v96
	v_exp_f32_e32 v8, v122
	v_fma_f32 v123, v9, s16, -v97
	v_exp_f32_e32 v9, v123
	v_fma_f32 v120, v10, s16, -v98
	v_exp_f32_e32 v10, v120
	v_fma_f32 v121, v11, s16, -v99
	v_exp_f32_e32 v11, v121
	v_fma_f32 v122, v12, s16, -v100
	v_exp_f32_e32 v12, v122
	v_fma_f32 v123, v13, s16, -v101
	v_exp_f32_e32 v13, v123
	v_fma_f32 v120, v14, s16, -v102
	v_exp_f32_e32 v14, v120
	v_fma_f32 v121, v15, s16, -v103
	v_exp_f32_e32 v15, v121
	v_fma_f32 v122, v16, s16, -v104
	v_exp_f32_e32 v16, v122
	v_fma_f32 v123, v17, s16, -v105
	v_exp_f32_e32 v17, v123
	global_store_dword v116, v2, s[10:11] offset:0
	global_store_dword v116, v3, s[10:11] offset:788
	global_store_dword v116, v4, s[10:11] offset:1576
	global_store_dword v116, v5, s[10:11] offset:2364
	global_store_dword v117, v6, s[10:11] offset:0
	global_store_dword v117, v7, s[10:11] offset:788
	global_store_dword v117, v8, s[10:11] offset:1576
	global_store_dword v117, v9, s[10:11] offset:2364
	global_store_dword v118, v10, s[10:11] offset:0
	global_store_dword v118, v11, s[10:11] offset:788
	global_store_dword v118, v12, s[10:11] offset:1576
	global_store_dword v118, v13, s[10:11] offset:2364
	global_store_dword v119, v14, s[10:11] offset:0
	global_store_dword v119, v15, s[10:11] offset:788
	global_store_dword v119, v16, s[10:11] offset:1576
	global_store_dword v119, v17, s[10:11] offset:2364
	ds_read_b128 v[66:69], v112 offset:9216
	ds_read_b128 v[70:73], v112 offset:9248
	s_waitcnt lgkmcnt(1)
	v_mfma_f32_32x32x16_f16 v[2:17], v[74:77], v[66:69], 0
	ds_read_b128 v[66:69], v112 offset:9280
	s_waitcnt lgkmcnt(1)
	v_mfma_f32_32x32x16_f16 v[2:17], v[78:81], v[70:73], v[2:17]
	ds_read_b128 v[70:73], v112 offset:9312
	s_waitcnt lgkmcnt(1)
	v_mfma_f32_32x32x16_f16 v[2:17], v[82:85], v[66:69], v[2:17]
	s_waitcnt lgkmcnt(0)
	v_mfma_f32_32x32x16_f16 v[2:17], v[86:89], v[70:73], v[2:17]
	v_fma_f32 v120, v18, s16, -v90
	v_exp_f32_e32 v18, v120
	v_fma_f32 v121, v19, s16, -v91
	v_exp_f32_e32 v19, v121
	v_fma_f32 v122, v20, s16, -v92
	v_exp_f32_e32 v20, v122
	v_fma_f32 v123, v21, s16, -v93
	v_exp_f32_e32 v21, v123
	v_fma_f32 v120, v22, s16, -v94
	v_exp_f32_e32 v22, v120
	v_fma_f32 v121, v23, s16, -v95
	v_exp_f32_e32 v23, v121
	v_fma_f32 v122, v24, s16, -v96
	v_exp_f32_e32 v24, v122
	v_fma_f32 v123, v25, s16, -v97
	v_exp_f32_e32 v25, v123
	v_fma_f32 v120, v26, s16, -v98
	v_exp_f32_e32 v26, v120
	v_fma_f32 v121, v27, s16, -v99
	v_exp_f32_e32 v27, v121
	v_fma_f32 v122, v28, s16, -v100
	v_exp_f32_e32 v28, v122
	v_fma_f32 v123, v29, s16, -v101
	v_exp_f32_e32 v29, v123
	v_fma_f32 v120, v30, s16, -v102
	v_exp_f32_e32 v30, v120
	v_fma_f32 v121, v31, s16, -v103
	v_exp_f32_e32 v31, v121
	v_fma_f32 v122, v32, s16, -v104
	v_exp_f32_e32 v32, v122
	v_fma_f32 v123, v33, s16, -v105
	v_exp_f32_e32 v33, v123
	global_store_dword v116, v18, s[10:11] offset:128
	global_store_dword v116, v19, s[10:11] offset:916
	global_store_dword v116, v20, s[10:11] offset:1704
	global_store_dword v116, v21, s[10:11] offset:2492
	global_store_dword v117, v22, s[10:11] offset:128
	global_store_dword v117, v23, s[10:11] offset:916
	global_store_dword v117, v24, s[10:11] offset:1704
	global_store_dword v117, v25, s[10:11] offset:2492
	global_store_dword v118, v26, s[10:11] offset:128
	global_store_dword v118, v27, s[10:11] offset:916
	global_store_dword v118, v28, s[10:11] offset:1704
	global_store_dword v118, v29, s[10:11] offset:2492
	global_store_dword v119, v30, s[10:11] offset:128
	global_store_dword v119, v31, s[10:11] offset:916
	global_store_dword v119, v32, s[10:11] offset:1704
	global_store_dword v119, v33, s[10:11] offset:2492
	ds_read_b128 v[66:69], v112 offset:13824
	ds_read_b128 v[70:73], v112 offset:13856
	s_waitcnt lgkmcnt(1)
	v_mfma_f32_32x32x16_f16 v[18:33], v[74:77], v[66:69], 0
	ds_read_b128 v[66:69], v112 offset:13888
	s_waitcnt lgkmcnt(1)
	v_mfma_f32_32x32x16_f16 v[18:33], v[78:81], v[70:73], v[18:33]
	ds_read_b128 v[70:73], v112 offset:13920
	s_waitcnt lgkmcnt(1)
	v_mfma_f32_32x32x16_f16 v[18:33], v[82:85], v[66:69], v[18:33]
	s_waitcnt lgkmcnt(0)
	v_mfma_f32_32x32x16_f16 v[18:33], v[86:89], v[70:73], v[18:33]
	v_fma_f32 v120, v2, s16, -v90
	v_exp_f32_e32 v2, v120
	v_fma_f32 v121, v3, s16, -v91
	v_exp_f32_e32 v3, v121
	v_fma_f32 v122, v4, s16, -v92
	v_exp_f32_e32 v4, v122
	v_fma_f32 v123, v5, s16, -v93
	v_exp_f32_e32 v5, v123
	v_fma_f32 v120, v6, s16, -v94
	v_exp_f32_e32 v6, v120
	v_fma_f32 v121, v7, s16, -v95
	v_exp_f32_e32 v7, v121
	v_fma_f32 v122, v8, s16, -v96
	v_exp_f32_e32 v8, v122
	v_fma_f32 v123, v9, s16, -v97
	v_exp_f32_e32 v9, v123
	v_fma_f32 v120, v10, s16, -v98
	v_exp_f32_e32 v10, v120
	v_fma_f32 v121, v11, s16, -v99
	v_exp_f32_e32 v11, v121
	v_fma_f32 v122, v12, s16, -v100
	v_exp_f32_e32 v12, v122
	v_fma_f32 v123, v13, s16, -v101
	v_exp_f32_e32 v13, v123
	v_fma_f32 v120, v14, s16, -v102
	v_exp_f32_e32 v14, v120
	v_fma_f32 v121, v15, s16, -v103
	v_exp_f32_e32 v15, v121
	v_fma_f32 v122, v16, s16, -v104
	v_exp_f32_e32 v16, v122
	v_fma_f32 v123, v17, s16, -v105
	v_exp_f32_e32 v17, v123
	global_store_dword v116, v2, s[10:11] offset:256
	global_store_dword v116, v3, s[10:11] offset:1044
	global_store_dword v116, v4, s[10:11] offset:1832
	global_store_dword v116, v5, s[10:11] offset:2620
	global_store_dword v117, v6, s[10:11] offset:256
	global_store_dword v117, v7, s[10:11] offset:1044
	global_store_dword v117, v8, s[10:11] offset:1832
	global_store_dword v117, v9, s[10:11] offset:2620
	global_store_dword v118, v10, s[10:11] offset:256
	global_store_dword v118, v11, s[10:11] offset:1044
	global_store_dword v118, v12, s[10:11] offset:1832
	global_store_dword v118, v13, s[10:11] offset:2620
	global_store_dword v119, v14, s[10:11] offset:256
	global_store_dword v119, v15, s[10:11] offset:1044
	global_store_dword v119, v16, s[10:11] offset:1832
	global_store_dword v119, v17, s[10:11] offset:2620
	ds_read_b128 v[66:69], v112 offset:18432
	ds_read_b128 v[70:73], v112 offset:18464
	s_waitcnt lgkmcnt(1)
	v_mfma_f32_32x32x16_f16 v[2:17], v[74:77], v[66:69], 0
	ds_read_b128 v[66:69], v112 offset:18496
	s_waitcnt lgkmcnt(1)
	v_mfma_f32_32x32x16_f16 v[2:17], v[78:81], v[70:73], v[2:17]
	ds_read_b128 v[70:73], v112 offset:18528
	s_waitcnt lgkmcnt(1)
	v_mfma_f32_32x32x16_f16 v[2:17], v[82:85], v[66:69], v[2:17]
	s_waitcnt lgkmcnt(0)
	v_mfma_f32_32x32x16_f16 v[2:17], v[86:89], v[70:73], v[2:17]
	v_fma_f32 v120, v18, s16, -v90
	v_exp_f32_e32 v18, v120
	v_fma_f32 v121, v19, s16, -v91
	v_exp_f32_e32 v19, v121
	v_fma_f32 v122, v20, s16, -v92
	v_exp_f32_e32 v20, v122
	v_fma_f32 v123, v21, s16, -v93
	v_exp_f32_e32 v21, v123
	v_fma_f32 v120, v22, s16, -v94
	v_exp_f32_e32 v22, v120
	v_fma_f32 v121, v23, s16, -v95
	v_exp_f32_e32 v23, v121
	v_fma_f32 v122, v24, s16, -v96
	v_exp_f32_e32 v24, v122
	v_fma_f32 v123, v25, s16, -v97
	v_exp_f32_e32 v25, v123
	v_fma_f32 v120, v26, s16, -v98
	v_exp_f32_e32 v26, v120
	v_fma_f32 v121, v27, s16, -v99
	v_exp_f32_e32 v27, v121
	v_fma_f32 v122, v28, s16, -v100
	v_exp_f32_e32 v28, v122
	v_fma_f32 v123, v29, s16, -v101
	v_exp_f32_e32 v29, v123
	v_fma_f32 v120, v30, s16, -v102
	v_exp_f32_e32 v30, v120
	v_fma_f32 v121, v31, s16, -v103
	v_exp_f32_e32 v31, v121
	v_fma_f32 v122, v32, s16, -v104
	v_exp_f32_e32 v32, v122
	v_fma_f32 v123, v33, s16, -v105
	v_exp_f32_e32 v33, v123
	global_store_dword v116, v18, s[10:11] offset:384
	global_store_dword v116, v19, s[10:11] offset:1172
	global_store_dword v116, v20, s[10:11] offset:1960
	global_store_dword v116, v21, s[10:11] offset:2748
	global_store_dword v117, v22, s[10:11] offset:384
	global_store_dword v117, v23, s[10:11] offset:1172
	global_store_dword v117, v24, s[10:11] offset:1960
	global_store_dword v117, v25, s[10:11] offset:2748
	global_store_dword v118, v26, s[10:11] offset:384
	global_store_dword v118, v27, s[10:11] offset:1172
	global_store_dword v118, v28, s[10:11] offset:1960
	global_store_dword v118, v29, s[10:11] offset:2748
	global_store_dword v119, v30, s[10:11] offset:384
	global_store_dword v119, v31, s[10:11] offset:1172
	global_store_dword v119, v32, s[10:11] offset:1960
	global_store_dword v119, v33, s[10:11] offset:2748
	ds_read_b128 v[66:69], v112 offset:23040
	ds_read_b128 v[70:73], v112 offset:23072
	s_waitcnt lgkmcnt(1)
	v_mfma_f32_32x32x16_f16 v[18:33], v[74:77], v[66:69], 0
	ds_read_b128 v[66:69], v112 offset:23104
	s_waitcnt lgkmcnt(1)
	v_mfma_f32_32x32x16_f16 v[18:33], v[78:81], v[70:73], v[18:33]
	ds_read_b128 v[70:73], v112 offset:23136
	s_waitcnt lgkmcnt(1)
	v_mfma_f32_32x32x16_f16 v[18:33], v[82:85], v[66:69], v[18:33]
	s_waitcnt lgkmcnt(0)
	v_mfma_f32_32x32x16_f16 v[18:33], v[86:89], v[70:73], v[18:33]
	v_fma_f32 v120, v2, s16, -v90
	v_exp_f32_e32 v2, v120
	v_fma_f32 v121, v3, s16, -v91
	v_exp_f32_e32 v3, v121
	v_fma_f32 v122, v4, s16, -v92
	v_exp_f32_e32 v4, v122
	v_fma_f32 v123, v5, s16, -v93
	v_exp_f32_e32 v5, v123
	v_fma_f32 v120, v6, s16, -v94
	v_exp_f32_e32 v6, v120
	v_fma_f32 v121, v7, s16, -v95
	v_exp_f32_e32 v7, v121
	v_fma_f32 v122, v8, s16, -v96
	v_exp_f32_e32 v8, v122
	v_fma_f32 v123, v9, s16, -v97
	v_exp_f32_e32 v9, v123
	v_fma_f32 v120, v10, s16, -v98
	v_exp_f32_e32 v10, v120
	v_fma_f32 v121, v11, s16, -v99
	v_exp_f32_e32 v11, v121
	v_fma_f32 v122, v12, s16, -v100
	v_exp_f32_e32 v12, v122
	v_fma_f32 v123, v13, s16, -v101
	v_exp_f32_e32 v13, v123
	v_fma_f32 v120, v14, s16, -v102
	v_exp_f32_e32 v14, v120
	v_fma_f32 v121, v15, s16, -v103
	v_exp_f32_e32 v15, v121
	v_fma_f32 v122, v16, s16, -v104
	v_exp_f32_e32 v16, v122
	v_fma_f32 v123, v17, s16, -v105
	v_exp_f32_e32 v17, v123
	global_store_dword v116, v2, s[10:11] offset:512
	global_store_dword v116, v3, s[10:11] offset:1300
	global_store_dword v116, v4, s[10:11] offset:2088
	global_store_dword v116, v5, s[10:11] offset:2876
	global_store_dword v117, v6, s[10:11] offset:512
	global_store_dword v117, v7, s[10:11] offset:1300
	global_store_dword v117, v8, s[10:11] offset:2088
	global_store_dword v117, v9, s[10:11] offset:2876
	global_store_dword v118, v10, s[10:11] offset:512
	global_store_dword v118, v11, s[10:11] offset:1300
	global_store_dword v118, v12, s[10:11] offset:2088
	global_store_dword v118, v13, s[10:11] offset:2876
	global_store_dword v119, v14, s[10:11] offset:512
	global_store_dword v119, v15, s[10:11] offset:1300
	global_store_dword v119, v16, s[10:11] offset:2088
	global_store_dword v119, v17, s[10:11] offset:2876
	ds_read_b128 v[66:69], v112 offset:27648
	ds_read_b128 v[70:73], v112 offset:27680
	s_waitcnt lgkmcnt(1)
	v_mfma_f32_32x32x16_f16 v[2:17], v[74:77], v[66:69], 0
	ds_read_b128 v[66:69], v112 offset:27712
	s_waitcnt lgkmcnt(1)
	v_mfma_f32_32x32x16_f16 v[2:17], v[78:81], v[70:73], v[2:17]
	ds_read_b128 v[70:73], v112 offset:27744
	s_waitcnt lgkmcnt(1)
	v_mfma_f32_32x32x16_f16 v[2:17], v[82:85], v[66:69], v[2:17]
	s_waitcnt lgkmcnt(0)
	v_mfma_f32_32x32x16_f16 v[2:17], v[86:89], v[70:73], v[2:17]
	v_fma_f32 v120, v18, s16, -v90
	v_exp_f32_e32 v18, v120
	v_fma_f32 v121, v19, s16, -v91
	v_exp_f32_e32 v19, v121
	v_fma_f32 v122, v20, s16, -v92
	v_exp_f32_e32 v20, v122
	v_fma_f32 v123, v21, s16, -v93
	v_exp_f32_e32 v21, v123
	v_fma_f32 v120, v22, s16, -v94
	v_exp_f32_e32 v22, v120
	v_fma_f32 v121, v23, s16, -v95
	v_exp_f32_e32 v23, v121
	v_fma_f32 v122, v24, s16, -v96
	v_exp_f32_e32 v24, v122
	v_fma_f32 v123, v25, s16, -v97
	v_exp_f32_e32 v25, v123
	v_fma_f32 v120, v26, s16, -v98
	v_exp_f32_e32 v26, v120
	v_fma_f32 v121, v27, s16, -v99
	v_exp_f32_e32 v27, v121
	v_fma_f32 v122, v28, s16, -v100
	v_exp_f32_e32 v28, v122
	v_fma_f32 v123, v29, s16, -v101
	v_exp_f32_e32 v29, v123
	v_fma_f32 v120, v30, s16, -v102
	v_exp_f32_e32 v30, v120
	v_fma_f32 v121, v31, s16, -v103
	v_exp_f32_e32 v31, v121
	v_fma_f32 v122, v32, s16, -v104
	v_exp_f32_e32 v32, v122
	v_fma_f32 v123, v33, s16, -v105
	v_exp_f32_e32 v33, v123
	global_store_dword v116, v18, s[10:11] offset:640
	global_store_dword v116, v19, s[10:11] offset:1428
	global_store_dword v116, v20, s[10:11] offset:2216
	global_store_dword v116, v21, s[10:11] offset:3004
	global_store_dword v117, v22, s[10:11] offset:640
	global_store_dword v117, v23, s[10:11] offset:1428
	global_store_dword v117, v24, s[10:11] offset:2216
	global_store_dword v117, v25, s[10:11] offset:3004
	global_store_dword v118, v26, s[10:11] offset:640
	global_store_dword v118, v27, s[10:11] offset:1428
	global_store_dword v118, v28, s[10:11] offset:2216
	global_store_dword v118, v29, s[10:11] offset:3004
	global_store_dword v119, v30, s[10:11] offset:640
	global_store_dword v119, v31, s[10:11] offset:1428
	global_store_dword v119, v32, s[10:11] offset:2216
	global_store_dword v119, v33, s[10:11] offset:3004
	s_nop 15
	s_nop 1
	v_fma_f32 v120, v2, s16, -v90
	v_exp_f32_e32 v2, v120
	v_fma_f32 v121, v3, s16, -v91
	v_exp_f32_e32 v3, v121
	v_fma_f32 v122, v4, s16, -v92
	v_exp_f32_e32 v4, v122
	v_fma_f32 v123, v5, s16, -v93
	v_exp_f32_e32 v5, v123
	v_fma_f32 v120, v6, s16, -v94
	v_exp_f32_e32 v6, v120
	v_fma_f32 v121, v7, s16, -v95
	v_exp_f32_e32 v7, v121
	v_fma_f32 v122, v8, s16, -v96
	v_exp_f32_e32 v8, v122
	v_fma_f32 v123, v9, s16, -v97
	v_exp_f32_e32 v9, v123
	v_fma_f32 v120, v10, s16, -v98
	v_exp_f32_e32 v10, v120
	v_fma_f32 v121, v11, s16, -v99
	v_exp_f32_e32 v11, v121
	v_fma_f32 v122, v12, s16, -v100
	v_exp_f32_e32 v12, v122
	v_fma_f32 v123, v13, s16, -v101
	v_exp_f32_e32 v13, v123
	v_fma_f32 v120, v14, s16, -v102
	v_exp_f32_e32 v14, v120
	v_fma_f32 v121, v15, s16, -v103
	v_exp_f32_e32 v15, v121
	v_fma_f32 v122, v16, s16, -v104
	v_exp_f32_e32 v16, v122
	v_fma_f32 v123, v17, s16, -v105
	v_exp_f32_e32 v17, v123
	s_and_b64 exec, exec, s[22:23]
	global_store_dword v116, v2, s[10:11] offset:768
	global_store_dword v116, v3, s[10:11] offset:1556
	global_store_dword v116, v4, s[10:11] offset:2344
	global_store_dword v116, v5, s[10:11] offset:3132
	global_store_dword v117, v6, s[10:11] offset:768
	global_store_dword v117, v7, s[10:11] offset:1556
	global_store_dword v117, v8, s[10:11] offset:2344
	global_store_dword v117, v9, s[10:11] offset:3132
	global_store_dword v118, v10, s[10:11] offset:768
	global_store_dword v118, v11, s[10:11] offset:1556
	global_store_dword v118, v12, s[10:11] offset:2344
	global_store_dword v118, v13, s[10:11] offset:3132
	global_store_dword v119, v14, s[10:11] offset:768
	global_store_dword v119, v15, s[10:11] offset:1556
	global_store_dword v119, v16, s[10:11] offset:2344
	global_store_dword v119, v17, s[10:11] offset:3132
	s_mov_b64 exec, s[18:19]
	s_endpgm
.Lsp_wave6:
	ds_read_b128 v[66:69], v112 offset:0
	ds_read_b128 v[70:73], v112 offset:32
	s_waitcnt lgkmcnt(1)
	v_mfma_f32_32x32x16_f16 v[2:17], v[74:77], v[66:69], 0
	ds_read_b128 v[66:69], v112 offset:64
	s_waitcnt lgkmcnt(1)
	v_mfma_f32_32x32x16_f16 v[2:17], v[78:81], v[70:73], v[2:17]
	ds_read_b128 v[70:73], v112 offset:96
	s_waitcnt lgkmcnt(1)
	v_mfma_f32_32x32x16_f16 v[2:17], v[82:85], v[66:69], v[2:17]
	s_waitcnt lgkmcnt(0)
	v_mfma_f32_32x32x16_f16 v[2:17], v[86:89], v[70:73], v[2:17]
	s_waitcnt lgkmcnt(0)
	ds_read_b128 v[66:69], v112 offset:4608
	ds_read_b128 v[70:73], v112 offset:4640
	s_waitcnt lgkmcnt(1)
	v_mfma_f32_32x32x16_f16 v[18:33], v[74:77], v[66:69], 0
	ds_read_b128 v[66:69], v112 offset:4672
	s_waitcnt lgkmcnt(1)
	v_mfma_f32_32x32x16_f16 v[18:33], v[78:81], v[70:73], v[18:33]
	ds_read_b128 v[70:73], v112 offset:4704
	s_waitcnt lgkmcnt(1)
	v_mfma_f32_32x32x16_f16 v[18:33], v[82:85], v[66:69], v[18:33]
	s_waitcnt lgkmcnt(0)
	v_mfma_f32_32x32x16_f16 v[18:33], v[86:89], v[70:73], v[18:33]
	v_fma_f32 v120, v2, s16, -v90
	v_exp_f32_e32 v2, v120
	v_fma_f32 v121, v3, s16, -v91
	v_exp_f32_e32 v3, v121
	v_fma_f32 v122, v4, s16, -v92
	v_exp_f32_e32 v4, v122
	v_fma_f32 v123, v5, s16, -v93
	v_exp_f32_e32 v5, v123
	global_store_dword v116, v2, s[10:11] offset:0
	s_and_b64 exec, exec, s[14:15]
	global_store_dword v116, v3, s[10:11] offset:788
	global_store_dword v116, v4, s[10:11] offset:1576
	global_store_dword v116, v5, s[10:11] offset:2364
	s_mov_b64 exec, s[18:19]
	ds_read_b128 v[66:69], v112 offset:9216
	ds_read_b128 v[70:73], v112 offset:9248
	s_waitcnt lgkmcnt(1)
	v_mfma_f32_32x32x16_f16 v[2:17], v[74:77], v[66:69], 0
	ds_read_b128 v[66:69], v112 offset:9280
	s_waitcnt lgkmcnt(1)
	v_mfma_f32_32x32x16_f16 v[2:17], v[78:81], v[70:73], v[2:17]
	ds_read_b128 v[70:73], v112 offset:9312
	s_waitcnt lgkmcnt(1)
	v_mfma_f32_32x32x16_f16 v[2:17], v[82:85], v[66:69], v[2:17]
	s_waitcnt lgkmcnt(0)
	v_mfma_f32_32x32x16_f16 v[2:17], v[86:89], v[70:73], v[2:17]
	v_fma_f32 v120, v18, s16, -v90
	v_exp_f32_e32 v18, v120
	v_fma_f32 v121, v19, s16, -v91
	v_exp_f32_e32 v19, v121
	v_fma_f32 v122, v20, s16, -v92
	v_exp_f32_e32 v20, v122
	v_fma_f32 v123, v21, s16, -v93
	v_exp_f32_e32 v21, v123
	global_store_dword v116, v18, s[10:11] offset:128
	s_and_b64 exec, exec, s[14:15]
	global_store_dword v116, v19, s[10:11] offset:916
	global_store_dword v116, v20, s[10:11] offset:1704
	global_store_dword v116, v21, s[10:11] offset:2492
	s_mov_b64 exec, s[18:19]
	ds_read_b128 v[66:69], v112 offset:13824
	ds_read_b128 v[70:73], v112 offset:13856
	s_waitcnt lgkmcnt(1)
	v_mfma_f32_32x32x16_f16 v[18:33], v[74:77], v[66:69], 0
	ds_read_b128 v[66:69], v112 offset:13888
	s_waitcnt lgkmcnt(1)
	v_mfma_f32_32x32x16_f16 v[18:33], v[78:81], v[70:73], v[18:33]
	ds_read_b128 v[70:73], v112 offset:13920
	s_waitcnt lgkmcnt(1)
	v_mfma_f32_32x32x16_f16 v[18:33], v[82:85], v[66:69], v[18:33]
	s_waitcnt lgkmcnt(0)
	v_mfma_f32_32x32x16_f16 v[18:33], v[86:89], v[70:73], v[18:33]
	v_fma_f32 v120, v2, s16, -v90
	v_exp_f32_e32 v2, v120
	v_fma_f32 v121, v3, s16, -v91
	v_exp_f32_e32 v3, v121
	v_fma_f32 v122, v4, s16, -v92
	v_exp_f32_e32 v4, v122
	v_fma_f32 v123, v5, s16, -v93
	v_exp_f32_e32 v5, v123
	global_store_dword v116, v2, s[10:11] offset:256
	s_and_b64 exec, exec, s[14:15]
	global_store_dword v116, v3, s[10:11] offset:1044
	global_store_dword v116, v4, s[10:11] offset:1832
	global_store_dword v116, v5, s[10:11] offset:2620
	s_mov_b64 exec, s[18:19]
	ds_read_b128 v[66:69], v112 offset:18432
	ds_read_b128 v[70:73], v112 offset:18464
	s_waitcnt lgkmcnt(1)
	v_mfma_f32_32x32x16_f16 v[2:17], v[74:77], v[66:69], 0
	ds_read_b128 v[66:69], v112 offset:18496
	s_waitcnt lgkmcnt(1)
	v_mfma_f32_32x32x16_f16 v[2:17], v[78:81], v[70:73], v[2:17]
	ds_read_b128 v[70:73], v112 offset:18528
	s_waitcnt lgkmcnt(1)
	v_mfma_f32_32x32x16_f16 v[2:17], v[82:85], v[66:69], v[2:17]
	s_waitcnt lgkmcnt(0)
	v_mfma_f32_32x32x16_f16 v[2:17], v[86:89], v[70:73], v[2:17]
	v_fma_f32 v120, v18, s16, -v90
	v_exp_f32_e32 v18, v120
	v_fma_f32 v121, v19, s16, -v91
	v_exp_f32_e32 v19, v121
	v_fma_f32 v122, v20, s16, -v92
	v_exp_f32_e32 v20, v122
	v_fma_f32 v123, v21, s16, -v93
	v_exp_f32_e32 v21, v123
	global_store_dword v116, v18, s[10:11] offset:384
	s_and_b64 exec, exec, s[14:15]
	global_store_dword v116, v19, s[10:11] offset:1172
	global_store_dword v116, v20, s[10:11] offset:1960
	global_store_dword v116, v21, s[10:11] offset:2748
	s_mov_b64 exec, s[18:19]
	ds_read_b128 v[66:69], v112 offset:23040
	ds_read_b128 v[70:73], v112 offset:23072
	s_waitcnt lgkmcnt(1)
	v_mfma_f32_32x32x16_f16 v[18:33], v[74:77], v[66:69], 0
	ds_read_b128 v[66:69], v112 offset:23104
	s_waitcnt lgkmcnt(1)
	v_mfma_f32_32x32x16_f16 v[18:33], v[78:81], v[70:73], v[18:33]
	ds_read_b128 v[70:73], v112 offset:23136
	s_waitcnt lgkmcnt(1)
	v_mfma_f32_32x32x16_f16 v[18:33], v[82:85], v[66:69], v[18:33]
	s_waitcnt lgkmcnt(0)
	v_mfma_f32_32x32x16_f16 v[18:33], v[86:89], v[70:73], v[18:33]
	v_fma_f32 v120, v2, s16, -v90
	v_exp_f32_e32 v2, v120
	v_fma_f32 v121, v3, s16, -v91
	v_exp_f32_e32 v3, v121
	v_fma_f32 v122, v4, s16, -v92
	v_exp_f32_e32 v4, v122
	v_fma_f32 v123, v5, s16, -v93
	v_exp_f32_e32 v5, v123
	global_store_dword v116, v2, s[10:11] offset:512
	s_and_b64 exec, exec, s[14:15]
	global_store_dword v116, v3, s[10:11] offset:1300
	global_store_dword v116, v4, s[10:11] offset:2088
	global_store_dword v116, v5, s[10:11] offset:2876
	s_mov_b64 exec, s[18:19]
	ds_read_b128 v[66:69], v112 offset:27648
	ds_read_b128 v[70:73], v112 offset:27680
	s_waitcnt lgkmcnt(1)
	v_mfma_f32_32x32x16_f16 v[2:17], v[74:77], v[66:69], 0
	ds_read_b128 v[66:69], v112 offset:27712
	s_waitcnt lgkmcnt(1)
	v_mfma_f32_32x32x16_f16 v[2:17], v[78:81], v[70:73], v[2:17]
	ds_read_b128 v[70:73], v112 offset:27744
	s_waitcnt lgkmcnt(1)
	v_mfma_f32_32x32x16_f16 v[2:17], v[82:85], v[66:69], v[2:17]
	s_waitcnt lgkmcnt(0)
	v_mfma_f32_32x32x16_f16 v[2:17], v[86:89], v[70:73], v[2:17]
	v_fma_f32 v120, v18, s16, -v90
	v_exp_f32_e32 v18, v120
	v_fma_f32 v121, v19, s16, -v91
	v_exp_f32_e32 v19, v121
	v_fma_f32 v122, v20, s16, -v92
	v_exp_f32_e32 v20, v122
	v_fma_f32 v123, v21, s16, -v93
	v_exp_f32_e32 v21, v123
	global_store_dword v116, v18, s[10:11] offset:640
	s_and_b64 exec, exec, s[14:15]
	global_store_dword v116, v19, s[10:11] offset:1428
	global_store_dword v116, v20, s[10:11] offset:2216
	global_store_dword v116, v21, s[10:11] offset:3004
	s_mov_b64 exec, s[18:19]
	s_nop 15
	s_nop 1
	v_fma_f32 v120, v2, s16, -v90
	v_exp_f32_e32 v2, v120
	v_fma_f32 v121, v3, s16, -v91
	v_exp_f32_e32 v3, v121
	v_fma_f32 v122, v4, s16, -v92
	v_exp_f32_e32 v4, v122
	v_fma_f32 v123, v5, s16, -v93
	v_exp_f32_e32 v5, v123
	s_and_b64 exec, exec, s[22:23]
	global_store_dword v116, v2, s[10:11] offset:768
	s_and_b64 exec, exec, s[14:15]
	global_store_dword v116, v3, s[10:11] offset:1556
	global_store_dword v116, v4, s[10:11] offset:2344
	global_store_dword v116, v5, s[10:11] offset:3132
	s_mov_b64 exec, s[18:19]
	s_endpgm

	.amdhsa_kernel _Z9k_spatialPKDF16_S0_S0_PfPDF16_
		.amdhsa_group_segment_fixed_size 62336
		.amdhsa_private_segment_fixed_size 0
		.amdhsa_kernarg_size 40
		.amdhsa_user_sgpr_count 2
		.amdhsa_user_sgpr_dispatch_ptr 0
		.amdhsa_user_sgpr_queue_ptr 0
		.amdhsa_user_sgpr_kernarg_segment_ptr 1
		.amdhsa_user_sgpr_dispatch_id 0
		.amdhsa_user_sgpr_kernarg_preload_length 0
		.amdhsa_user_sgpr_kernarg_preload_offset 0
		.amdhsa_user_sgpr_private_segment_size 0
		.amdhsa_uses_dynamic_stack 0
		.amdhsa_enable_private_segment 0
		.amdhsa_system_sgpr_workgroup_id_x 1
		.amdhsa_system_sgpr_workgroup_id_y 0
		.amdhsa_system_sgpr_workgroup_id_z 0
		.amdhsa_system_sgpr_workgroup_info 0
		.amdhsa_system_vgpr_workitem_id 0
		.amdhsa_next_free_vgpr 128
		.amdhsa_next_free_sgpr 96
		.amdhsa_accum_offset 128
		.amdhsa_reserve_vcc 1
		.amdhsa_float_round_mode_32 0
		.amdhsa_float_round_mode_16_64 0
		.amdhsa_float_denorm_mode_32 3
		.amdhsa_float_denorm_mode_16_64 3
		.amdhsa_dx10_clamp 1
		.amdhsa_ieee_mode 1
		.amdhsa_fp16_overflow 0
		.amdhsa_tg_split 0
		.amdhsa_exception_fp_ieee_invalid_op 0
		.amdhsa_exception_fp_denorm_src 0
		.amdhsa_exception_fp_ieee_div_zero 0
		.amdhsa_exception_fp_ieee_overflow 0
		.amdhsa_exception_fp_ieee_underflow 0
		.amdhsa_exception_fp_ieee_inexact 0
		.amdhsa_exception_int_div_zero 0
	.end_amdhsa_kernel

amdhsa.kernels:
  - .agpr_count:     0
    .args:
      - .actual_access:  read_only
        .address_space:  global
        .offset:         0
        .size:           8
        .value_kind:     global_buffer
      - .actual_access:  read_only
        .address_space:  global
        .offset:         8
        .size:           8
        .value_kind:     global_buffer
      - .actual_access:  read_only
        .address_space:  global
        .offset:         16
        .size:           8
        .value_kind:     global_buffer
      - .actual_access:  write_only
        .address_space:  global
        .offset:         24
        .size:           8
        .value_kind:     global_buffer
      - .actual_access:  write_only
        .address_space:  global
        .offset:         32
        .size:           8
        .value_kind:     global_buffer
      - .actual_access:  write_only
        .address_space:  global
        .offset:         40
        .size:           8
        .value_kind:     global_buffer
      - .actual_access:  write_only
        .address_space:  global
        .offset:         48
        .size:           8
        .value_kind:     global_buffer
    .group_segment_fixed_size: 0
    .kernarg_segment_align: 8
    .kernarg_segment_size: 56
    .language:       OpenCL C
    .language_version:
      - 2
      - 0
    .max_flat_workgroup_size: 256
    .name:           _Z6k_prepPKfS0_S0_PDF16_S1_S1_Pi
    .private_segment_fixed_size: 0
    .sgpr_count:     16
    .sgpr_spill_count: 0
    .symbol:         _Z6k_prepPKfS0_S0_PDF16_S1_S1_Pi.kd
    .uniform_work_group_size: 1
    .uses_dynamic_stack: false
    .vgpr_count:     14
    .vgpr_spill_count: 0
    .wavefront_size: 64
  - .agpr_count:     0
    .args:
      - .address_space:  global
        .offset:         0
        .size:           8
        .value_kind:     global_buffer
      - .address_space:  global
        .offset:         8
        .size:           8
        .value_kind:     global_buffer
      - .actual_access:  read_only
        .address_space:  global
        .offset:         16
        .size:           8
        .value_kind:     global_buffer
      - .actual_access:  write_only
        .address_space:  global
        .offset:         24
        .size:           8
        .value_kind:     global_buffer
      - .actual_access:  write_only
        .address_space:  global
        .offset:         32
        .size:           8
        .value_kind:     global_buffer
      - .actual_access:  write_only
        .address_space:  global
        .offset:         40
        .size:           8
        .value_kind:     global_buffer
      - .actual_access:  write_only
        .address_space:  global
        .offset:         48
        .size:           8
        .value_kind:     global_buffer
      - .address_space:  global
        .offset:         56
        .size:           8
        .value_kind:     global_buffer
    .group_segment_fixed_size: 41984
    .kernarg_segment_align: 8
    .kernarg_segment_size: 64
    .language:       OpenCL C
    .language_version:
      - 2
      - 0
    .max_flat_workgroup_size: 256
    .name:           _Z14k_qkv_temporalPKDF16_S0_PKfPDF16_S3_S3_PfPi
    .private_segment_fixed_size: 0
    .sgpr_count:     29
    .sgpr_spill_count: 0
    .symbol:         _Z14k_qkv_temporalPKDF16_S0_PKfPDF16_S3_S3_PfPi.kd
    .uniform_work_group_size: 1
    .uses_dynamic_stack: false
    .vgpr_count:     168
    .vgpr_spill_count: 0
    .wavefront_size: 64
  - .agpr_count:     8
    .args:
      - .actual_access:  read_only
        .address_space:  global
        .offset:         0
        .size:           8
        .value_kind:     global_buffer
      - .actual_access:  read_only
        .address_space:  global
        .offset:         8
        .size:           8
        .value_kind:     global_buffer
      - .actual_access:  read_only
        .address_space:  global
        .offset:         16
        .size:           8
        .value_kind:     global_buffer
      - .actual_access:  write_only
        .address_space:  global
        .offset:         24
        .size:           8
        .value_kind:     global_buffer
      - .actual_access:  write_only
        .address_space:  global
        .offset:         32
        .size:           8
        .value_kind:     global_buffer
      - .actual_access:  write_only
        .address_space:  global
        .offset:         40
        .size:           8
        .value_kind:     global_buffer
      - .address_space:  global
        .offset:         48
        .size:           8
        .value_kind:     global_buffer
      - .actual_access:  read_only
        .address_space:  global
        .offset:         56
        .size:           8
        .value_kind:     global_buffer
      - .offset:         64
        .size:           4
        .value_kind:     hidden_block_count_x
      - .offset:         68
        .size:           4
        .value_kind:     hidden_block_count_y
      - .offset:         72
        .size:           4
        .value_kind:     hidden_block_count_z
      - .offset:         76
        .size:           2
        .value_kind:     hidden_group_size_x
      - .offset:         78
        .size:           2
        .value_kind:     hidden_group_size_y
      - .offset:         80
        .size:           2
        .value_kind:     hidden_group_size_z
      - .offset:         82
        .size:           2
        .value_kind:     hidden_remainder_x
      - .offset:         84
        .size:           2
        .value_kind:     hidden_remainder_y
      - .offset:         86
        .size:           2
        .value_kind:     hidden_remainder_z
      - .offset:         104
        .size:           8
        .value_kind:     hidden_global_offset_x
      - .offset:         112
        .size:           8
        .value_kind:     hidden_global_offset_y
      - .offset:         120
        .size:           8
        .value_kind:     hidden_global_offset_z
      - .offset:         128
        .size:           2
        .value_kind:     hidden_grid_dims
    .group_segment_fixed_size: 9568
    .kernarg_segment_align: 8
    .kernarg_segment_size: 320
    .language:       OpenCL C
    .language_version:
      - 2
      - 0
    .max_flat_workgroup_size: 256
    .name:           _Z7k_fixupPKfS0_S0_PDF16_S1_S1_PfPKi
    .private_segment_fixed_size: 0
    .sgpr_count:     96
    .sgpr_spill_count: 0
    .symbol:         _Z7k_fixupPKfS0_S0_PDF16_S1_S1_PfPKi.kd
    .uniform_work_group_size: 1
    .uses_dynamic_stack: false
    .vgpr_count:     164
    .vgpr_spill_count: 0
    .wavefront_size: 64
  - .agpr_count:     0
    .args:
      - .actual_access:  read_only
        .address_space:  global
        .offset:         0
        .size:           8
        .value_kind:     global_buffer
      - .actual_access:  read_only
        .address_space:  global
        .offset:         8
        .size:           8
        .value_kind:     global_buffer
      - .actual_access:  read_only
        .address_space:  global
        .offset:         16
        .size:           8
        .value_kind:     global_buffer
      - .actual_access:  write_only
        .address_space:  global
        .offset:         24
        .size:           8
        .value_kind:     global_buffer
      - .actual_access:  write_only
        .address_space:  global
        .offset:         32
        .size:           8
        .value_kind:     global_buffer
    .group_segment_fixed_size: 62336
    .kernarg_segment_align: 8
    .kernarg_segment_size: 40
    .language:       OpenCL C
    .language_version:
      - 2
      - 0
    .max_flat_workgroup_size: 448
    .name:           _Z9k_spatialPKDF16_S0_S0_PfPDF16_
    .private_segment_fixed_size: 0
    .sgpr_count:     19
    .sgpr_spill_count: 0
    .symbol:         _Z9k_spatialPKDF16_S0_S0_PfPDF16_.kd
    .uniform_work_group_size: 1
    .uses_dynamic_stack: false
    .vgpr_count:     128
    .vgpr_spill_count: 0
    .wavefront_size: 64
  - .agpr_count:     0
    .args:
      - .address_space:  global
        .offset:         0
        .size:           8
        .value_kind:     global_buffer
      - .address_space:  global
        .offset:         8
        .size:           8
        .value_kind:     global_buffer
      - .actual_access:  read_only
        .address_space:  global
        .offset:         16
        .size:           8
        .value_kind:     global_buffer
      - .actual_access:  write_only
        .address_space:  global
        .offset:         24
        .size:           8
        .value_kind:     global_buffer
    .group_segment_fixed_size: 65536
    .kernarg_segment_align: 8
    .kernarg_segment_size: 32
    .language:       OpenCL C
    .language_version:
      - 2
      - 0
    .max_flat_workgroup_size: 256
    .name:           _Z9k_outprojPKDF16_S0_PKfPf
    .private_segment_fixed_size: 0
    .sgpr_count:     28
    .sgpr_spill_count: 0
    .symbol:         _Z9k_outprojPKDF16_S0_PKfPf.kd
    .uniform_work_group_size: 1
    .uses_dynamic_stack: false
    .vgpr_count:     107
    .vgpr_spill_count: 0
    .wavefront_size: 64
